# W12 with plain (non-nt) stores in the in-proj epilogue only: Z is re-read by the mixer phases
# speedup vs baseline: 1.0053x; 1.0053x over previous
.LBB0_314:
	s_mov_b32 s0, -1
	v_mov_b32_e32 v195, 4
	v_mbcnt_lo_u32_b32 v40, s0, 0
	v_mbcnt_hi_u32_b32 v41, s0, v40
	s_lshl_b32 s0, s22, 8
	v_lshrrev_b32_e32 v40, 4, v41
	s_or_b32 s0, s0, s85
	v_lshl_add_u32 v193, v40, 3, s0
	s_movk_i32 s0, 0xc00
	v_mul_hi_i32 v42, v193, s6
	v_cmp_gt_i32_e64 s[42:43], s0, v193
	v_add_u32_e32 v203, 0xfffff400, v193
	v_mov_b32_e32 v196, 0x3000000
	v_lshrrev_b32_e32 v201, 31, v42
	v_lshrrev_b32_e32 v204, 7, v42
	v_mov_b32_e32 v200, 0x3000000
	v_mov_b32_e32 v202, 4
	s_and_saveexec_b64 s[0:1], s[42:43]
	v_add_u32_e32 v42, v204, v201
	s_mov_b32 s4, 0xc00000
	v_mul_lo_u32 v200, v42, s4
	v_mov_b32_e32 v202, 6
	v_mov_b32_e32 v203, v193
	s_or_b64 exec, exec, s[0:1]
	v_add_u32_e32 v194, 0x80, v193
	s_movk_i32 s0, 0xb80
	v_mul_hi_i32 v42, v194, s6
	v_cmp_gt_i32_e64 s[44:45], s0, v193
	v_add_u32_e32 v199, 0xfffff480, v193
	v_lshrrev_b32_e32 v197, 31, v42
	v_lshrrev_b32_e32 v198, 7, v42
	s_and_saveexec_b64 s[0:1], s[44:45]
	v_add_u32_e32 v42, v198, v197
	s_mov_b32 s4, 0xc00000
	v_mul_lo_u32 v196, v42, s4
	v_mov_b32_e32 v195, 6
	v_mov_b32_e32 v199, v194
	s_or_b64 exec, exec, s[0:1]
	s_lshl_b32 s8, s2, 8
	s_add_i32 s8, s8, s84
	s_cmp_lt_i32 s22, 6
	s_cselect_b64 s[80:81], -1, 0
	s_add_i32 s0, s22, -9
	s_sub_i32 s1, s22, 20
	s_min_u32 s0, s0, s1
	s_cmp_lt_u32 s0, 3
	v_and_b32_e32 v192, 15, v41
	s_cselect_b64 s[0:1], -1, 0
	s_and_b64 vcc, exec, s[80:81]
	s_cbranch_vccnz .Lepiz_m1
	s_and_b64 vcc, exec, s[0:1]
	s_cbranch_vccnz .Lepiz_m2
	v_cndmask_b32_e64 v172, 0, 1, s[80:81]
	v_cmp_ne_u32_e64 s[40:41], 1, v172
	s_mov_b64 s[4:5], -1
	v_cndmask_b32_e64 v159, 0, 1, s[0:1]
	v_cmp_ne_u32_e64 s[38:39], 1, v159
	v_mov_b32_e32 v156, v148
	v_mov_b32_e32 v179, v149
	v_mov_b32_e32 v180, v150
	v_mov_b32_e32 v182, v151
	v_mov_b32_e32 v178, v144
	v_mov_b32_e32 v185, v145
	v_mov_b32_e32 v186, v146
	v_mov_b32_e32 v188, v147
	s_lshr_b32 s0, s8, 4
	s_and_b32 s4, s0, 0xfc
	s_ashr_i32 s0, s2, 31
	s_lshr_b32 s0, s0, 28
	s_add_i32 s0, s2, s0
	s_ashr_i32 s13, s0, 4
	v_add_u32_e32 v144, v204, v201
	s_movk_i32 s0, 0x300
	v_mul_lo_u32 v144, v144, s0
	v_sub_u32_e32 v144, v193, v144
	v_cndmask_b32_e64 v146, v203, v144, s[42:43]
	v_lshrrev_b32_e32 v144, 7, v146
	v_mad_u64_u32 v[144:145], s[0:1], v202, s13, v[144:145]
	v_lshlrev_b32_e32 v145, 4, v146
	v_lshl_add_u32 v144, v144, 19, v200
	v_and_b32_e32 v145, 0x600, v145
	v_and_b32_e32 v146, 31, v146
	v_or3_b32 v146, v144, v145, v146
	v_add_u32_e32 v144, 0xfffff200, v193
	v_mul_hi_i32 v145, v144, s6
	v_lshrrev_b32_e32 v147, 31, v145
	v_ashrrev_i32_e32 v145, 6, v145
	v_add_u32_e32 v145, v145, v147
	v_mul_i32_i24_e32 v147, 0x180, v145
	v_sub_u32_e32 v144, v144, v147
	v_mul_i32_i24_e32 v147, 0x2aab, v144
	v_mov_b32_e32 v148, 4
	v_ashrrev_i16_sdwa v148, v148, v147 dst_sel:DWORD dst_unused:UNUSED_PAD src0_sel:DWORD src1_sel:WORD_1
	v_lshrrev_b32_e32 v147, 31, v147
	v_add_u16_e32 v147, v148, v147
	v_mul_lo_u16_e32 v148, 0x60, v147
	v_sub_u16_e32 v144, v144, v148
	s_lshl_b32 s5, s13, 2
	v_bfe_i32 v148, v144, 0, 16
	v_mul_i32_i24_e32 v144, 0x600000, v145
	v_and_or_b32 v144, v148, 31, v144
	v_add_u32_e32 v145, s5, v147
	s_mov_b32 s0, 0x60000
	v_lshlrev_b32_e32 v147, 4, v148
	v_mad_u64_u32 v[144:145], s[0:1], v145, s0, v[144:145]
	v_and_b32_e32 v147, 0xfffffe00, v147
	s_mov_b32 s0, 0x3800000
	v_add3_u32 v147, v144, v147, s0
	v_add_u32_e32 v144, 0xffffef00, v193
	v_mul_hi_i32 v145, v144, s6
	v_lshrrev_b32_e32 v148, 31, v145
	v_ashrrev_i32_e32 v145, 7, v145
	v_add_u32_e32 v145, v145, v148
	v_mul_i32_i24_e32 v148, 0x300, v145
	v_sub_u32_e32 v144, v144, v148
	v_mul_i32_i24_e32 v148, 0x2aab, v144
	v_mov_b32_e32 v149, 5
	v_ashrrev_i16_sdwa v149, v149, v148 dst_sel:DWORD dst_unused:UNUSED_PAD src0_sel:DWORD src1_sel:WORD_1
	v_lshrrev_b32_e32 v148, 31, v148
	v_add_u16_e32 v148, v149, v148
	v_mul_lo_u16_e32 v149, 0xc0, v148
	v_sub_u16_e32 v144, v144, v149
	s_mov_b32 s0, 0xc00000
	v_bfe_i32 v149, v144, 0, 16
	v_mul_lo_u32 v144, v145, s0
	v_and_or_b32 v144, v149, 31, v144
	v_add_u32_e32 v145, s5, v148
	s_mov_b32 s0, 0xc0000
	v_lshlrev_b32_e32 v148, 4, v149
	v_mad_u64_u32 v[144:145], s[0:1], v145, s0, v[144:145]
	v_and_b32_e32 v148, 0xfffffe00, v148
	s_mov_b32 s0, 0x4400000
	v_add3_u32 v144, v144, v148, s0
	s_movk_i32 s0, 0xe00
	s_lshl_b32 s2, s13, 16
	v_cmp_gt_i32_e32 vcc, s0, v193
	s_movk_i32 s0, 0x1710
	s_add_i32 s2, s2, 0x5bfe900
	v_cmp_gt_u32_e64 s[42:43], s0, v193
	s_movk_i32 s0, 0x1700
	v_add_u32_e32 v145, s2, v193
	v_cndmask_b32_e64 v149, 0, v237, s[42:43]
	v_cmp_gt_i32_e64 s[46:47], s0, v193
	s_movk_i32 s0, 0x1100
	v_cndmask_b32_e32 v148, v236, v218, vcc
	v_cndmask_b32_e64 v149, v149, v239, s[46:47]
	v_cmp_gt_i32_e64 s[42:43], s0, v193
	v_cndmask_b32_e64 v144, v145, v144, s[46:47]
	s_nop 0
	v_cndmask_b32_e64 v159, v149, v148, s[42:43]
	v_cndmask_b32_e64 v144, v144, v147, s[42:43]
	v_cndmask_b32_e32 v181, v144, v146, vcc
	v_cvt_pk_bf16_f32 v144, v156, v179
	v_cvt_pk_bf16_f32 v145, v180, v182
	v_cmp_ne_u32_e64 s[42:43], 0, v159
	v_cndmask_b32_e64 v180, 4, 5, s[46:47]
	v_cvt_pk_bf16_f32 v146, v178, v185
	v_cvt_pk_bf16_f32 v147, v186, v188
	s_and_saveexec_b64 s[0:1], s[42:43]
	v_mul_u32_u24_e32 v148, s4, v159
	v_lshl_or_b32 v148, v192, v180, v148
	v_add_u32_e32 v212, v148, v181
	v_lshl_add_u64 v[148:149], v[212:213], 1, s[52:53]
	global_store_dwordx4 v[148:149], v[144:147], off
	s_nop 1
	s_or_b64 exec, exec, s[0:1]
	s_mov_b64 s[0:1], -1
	v_mov_b32_e32 v144, v136
	v_mov_b32_e32 v145, v137
	v_mov_b32_e32 v146, v138
	v_mov_b32_e32 v148, v139
	v_mov_b32_e32 v147, v132
	v_mov_b32_e32 v151, v133
	v_mov_b32_e32 v178, v134
	v_mov_b32_e32 v156, v135
	v_add_u32_e32 v132, v198, v197
	s_movk_i32 s0, 0x300
	v_mul_lo_u32 v132, v132, s0
	v_sub_u32_e32 v132, v194, v132
	v_cndmask_b32_e64 v134, v199, v132, s[44:45]
	v_lshrrev_b32_e32 v132, 7, v134
	v_mad_u64_u32 v[132:133], s[0:1], v195, s13, v[132:133]
	v_lshlrev_b32_e32 v133, 4, v134
	v_lshl_add_u32 v132, v132, 19, v196
	v_and_b32_e32 v133, 0x600, v133
	v_and_b32_e32 v134, 31, v134
	v_or3_b32 v134, v132, v133, v134
	v_add_u32_e32 v132, 0xfffff280, v193
	v_mul_hi_i32 v133, v132, s6
	v_lshrrev_b32_e32 v135, 31, v133
	v_ashrrev_i32_e32 v133, 6, v133
	v_add_u32_e32 v133, v133, v135
	v_mul_i32_i24_e32 v135, 0x180, v133
	v_sub_u32_e32 v132, v132, v135
	v_mul_i32_i24_e32 v135, 0x2aab, v132
	v_lshrrev_b32_e32 v136, 31, v135
	v_ashrrev_i32_e32 v135, 20, v135
	v_add_u16_e32 v135, v135, v136
	v_mul_lo_u16_e32 v136, 0x60, v135
	v_sub_u16_e32 v132, v132, v136
	v_bfe_i32 v136, v132, 0, 16
	v_mul_i32_i24_e32 v132, 0x600000, v133
	v_and_or_b32 v132, v136, 31, v132
	v_add_u32_e32 v133, s5, v135
	s_mov_b32 s0, 0x60000
	v_lshlrev_b32_e32 v135, 4, v136
	v_mad_u64_u32 v[132:133], s[0:1], v133, s0, v[132:133]
	v_and_b32_e32 v135, 0xfffffe00, v135
	s_mov_b32 s0, 0x3800000
	v_add3_u32 v135, v132, v135, s0
	v_add_u32_e32 v132, 0xffffef80, v193
	v_mul_hi_i32 v133, v132, s6
	v_lshrrev_b32_e32 v136, 31, v133
	v_ashrrev_i32_e32 v133, 7, v133
	v_add_u32_e32 v133, v133, v136
	v_mul_i32_i24_e32 v136, 0x300, v133
	v_sub_u32_e32 v132, v132, v136
	v_mul_i32_i24_e32 v136, 0x2aab, v132
	v_lshrrev_b32_e32 v137, 31, v136
	v_ashrrev_i32_e32 v136, 21, v136
	v_add_u16_e32 v136, v136, v137
	v_mul_lo_u16_e32 v137, 0xc0, v136
	v_sub_u16_e32 v132, v132, v137
	s_mov_b32 s0, 0xc00000
	v_bfe_i32 v137, v132, 0, 16
	v_mul_lo_u32 v132, v133, s0
	v_and_or_b32 v132, v137, 31, v132
	v_add_u32_e32 v133, s5, v136
	s_mov_b32 s0, 0xc0000
	v_lshlrev_b32_e32 v136, 4, v137
	v_mad_u64_u32 v[132:133], s[0:1], v133, s0, v[132:133]
	v_and_b32_e32 v136, 0xfffffe00, v136
	s_mov_b32 s0, 0x4400000
	v_add3_u32 v132, v132, v136, s0
	s_movk_i32 s0, 0xd80
	v_cmp_gt_i32_e32 vcc, s0, v193
	s_movk_i32 s0, 0x1710
	v_cmp_gt_u32_e64 s[44:45], s0, v194
	s_movk_i32 s0, 0x1680
	v_add_u32_e32 v133, s2, v194
	v_cndmask_b32_e64 v137, 0, v237, s[44:45]
	v_cmp_gt_i32_e64 s[46:47], s0, v193
	s_movk_i32 s0, 0x1080
	v_cndmask_b32_e32 v136, v236, v218, vcc
	v_cndmask_b32_e64 v137, v137, v239, s[46:47]
	v_cmp_gt_i32_e64 s[44:45], s0, v193
	v_cndmask_b32_e64 v132, v133, v132, s[46:47]
	s_nop 0
	v_cndmask_b32_e64 v158, v137, v136, s[44:45]
	v_cndmask_b32_e64 v132, v132, v135, s[44:45]
	v_cndmask_b32_e32 v172, v132, v134, vcc
	v_cvt_pk_bf16_f32 v132, v144, v145
	v_cmp_ne_u32_e64 s[44:45], 0, v158
	v_cndmask_b32_e64 v145, 4, 5, s[46:47]
	v_cvt_pk_bf16_f32 v133, v146, v148
	v_cvt_pk_bf16_f32 v134, v147, v151
	v_cvt_pk_bf16_f32 v135, v178, v156
	s_and_saveexec_b64 s[0:1], s[44:45]
	v_mul_u32_u24_e32 v136, s4, v158
	v_lshl_or_b32 v136, v192, v145, v136
	v_add_u32_e32 v212, v136, v172
	v_lshl_add_u64 v[136:137], v[212:213], 1, s[52:53]
	global_store_dwordx4 v[136:137], v[132:135], off
	s_nop 1
	s_or_b64 exec, exec, s[0:1]
	s_or_b32 s2, s4, 1
	v_cvt_pk_bf16_f32 v127, v126, v127
	v_cvt_pk_bf16_f32 v126, v124, v125
	v_cvt_pk_bf16_f32 v124, v128, v129
	v_cvt_pk_bf16_f32 v125, v130, v131
	s_and_saveexec_b64 s[0:1], s[42:43]
	v_mul_u32_u24_e32 v128, s2, v159
	v_lshlrev_b32_e32 v129, v180, v192
	v_add3_u32 v212, v128, v129, v181
	v_lshl_add_u64 v[128:129], v[212:213], 1, s[52:53]
	global_store_dwordx4 v[128:129], v[124:127], off
	s_nop 1
	s_or_b64 exec, exec, s[0:1]
	v_cvt_pk_bf16_f32 v115, v114, v115
	v_cvt_pk_bf16_f32 v114, v112, v113
	v_cvt_pk_bf16_f32 v112, v116, v117
	v_cvt_pk_bf16_f32 v113, v118, v119
	s_and_saveexec_b64 s[0:1], s[44:45]
	v_mul_u32_u24_e32 v116, s2, v158
	v_lshlrev_b32_e32 v117, v145, v192
	v_add3_u32 v212, v116, v117, v172
	v_lshl_add_u64 v[116:117], v[212:213], 1, s[52:53]
	global_store_dwordx4 v[116:117], v[112:115], off
	s_nop 1
	s_or_b64 exec, exec, s[0:1]
	s_or_b32 s2, s4, 2
	v_cvt_pk_bf16_f32 v107, v106, v107
	v_cvt_pk_bf16_f32 v106, v104, v105
	v_cvt_pk_bf16_f32 v104, v108, v109
	v_cvt_pk_bf16_f32 v105, v110, v111
	s_and_saveexec_b64 s[0:1], s[42:43]
	v_mul_u32_u24_e32 v108, s2, v159
	v_lshl_or_b32 v108, v192, v180, v108
	v_add_u32_e32 v212, v108, v181
	v_lshl_add_u64 v[108:109], v[212:213], 1, s[52:53]
	global_store_dwordx4 v[108:109], v[104:107], off
	s_nop 1
	s_or_b64 exec, exec, s[0:1]
	v_cvt_pk_bf16_f32 v95, v94, v95
	v_cvt_pk_bf16_f32 v94, v92, v93
	v_cvt_pk_bf16_f32 v92, v96, v97
	v_cvt_pk_bf16_f32 v93, v98, v99
	s_and_saveexec_b64 s[0:1], s[44:45]
	v_mul_u32_u24_e32 v96, s2, v158
	v_lshl_or_b32 v96, v192, v145, v96
	v_add_u32_e32 v212, v96, v172
	v_lshl_add_u64 v[96:97], v[212:213], 1, s[52:53]
	global_store_dwordx4 v[96:97], v[92:95], off
	s_nop 1
	s_or_b64 exec, exec, s[0:1]
	s_or_b32 s2, s4, 3
	v_cvt_pk_bf16_f32 v87, v86, v87
	v_cvt_pk_bf16_f32 v86, v84, v85
	v_cvt_pk_bf16_f32 v84, v88, v89
	v_cvt_pk_bf16_f32 v85, v90, v91
	s_and_saveexec_b64 s[0:1], s[42:43]
	v_mul_u32_u24_e32 v88, s2, v159
	v_lshlrev_b32_e32 v89, v180, v192
	v_add3_u32 v212, v88, v89, v181
	v_lshl_add_u64 v[88:89], v[212:213], 1, s[52:53]
	global_store_dwordx4 v[88:89], v[84:87], off
	s_nop 1
	s_or_b64 exec, exec, s[0:1]
	v_cvt_pk_bf16_f32 v75, v74, v75
	v_cvt_pk_bf16_f32 v74, v72, v73
	v_cvt_pk_bf16_f32 v72, v76, v77
	v_cvt_pk_bf16_f32 v73, v78, v79
	s_and_saveexec_b64 s[0:1], s[44:45]
	v_mul_u32_u24_e32 v76, s2, v158
	v_lshlrev_b32_e32 v77, v145, v192
	v_add3_u32 v212, v76, v77, v172
	v_lshl_add_u64 v[76:77], v[212:213], 1, s[52:53]
	global_store_dwordx4 v[76:77], v[72:75], off
	s_nop 1
	s_or_b64 exec, exec, s[0:1]
	s_mov_b64 s[0:1], -1
	s_addk_i32 s8, 0x80
	s_lshr_b32 s0, s8, 4
	s_and_b32 s2, s0, 0xfc
	v_cvt_pk_bf16_f32 v67, v66, v67
	v_cvt_pk_bf16_f32 v66, v64, v65
	v_cvt_pk_bf16_f32 v64, v68, v69
	v_cvt_pk_bf16_f32 v65, v70, v71
	s_and_saveexec_b64 s[0:1], s[42:43]
	v_mul_u32_u24_e32 v68, s2, v159
	v_lshl_or_b32 v68, v192, v180, v68
	v_add_u32_e32 v212, v68, v181
	v_lshl_add_u64 v[68:69], v[212:213], 1, s[52:53]
	global_store_dwordx4 v[68:69], v[64:67], off
	s_nop 1
	s_or_b64 exec, exec, s[0:1]
	v_cvt_pk_bf16_f32 v55, v54, v55
	v_cvt_pk_bf16_f32 v54, v52, v53
	v_cvt_pk_bf16_f32 v52, v56, v57
	v_cvt_pk_bf16_f32 v53, v58, v59
	s_and_saveexec_b64 s[0:1], s[44:45]
	v_mul_u32_u24_e32 v56, s2, v158
	v_lshl_or_b32 v56, v192, v145, v56
	v_add_u32_e32 v212, v56, v172
	v_lshl_add_u64 v[56:57], v[212:213], 1, s[52:53]
	global_store_dwordx4 v[56:57], v[52:55], off
	s_nop 1
	s_or_b64 exec, exec, s[0:1]
	s_or_b32 s4, s2, 1
	v_cvt_pk_bf16_f32 v47, v46, v47
	v_cvt_pk_bf16_f32 v46, v44, v45
	v_cvt_pk_bf16_f32 v44, v48, v49
	v_cvt_pk_bf16_f32 v45, v50, v51
	s_and_saveexec_b64 s[0:1], s[42:43]
	v_mul_u32_u24_e32 v48, s4, v159
	v_lshlrev_b32_e32 v49, v180, v192
	v_add3_u32 v212, v48, v49, v181
	v_lshl_add_u64 v[48:49], v[212:213], 1, s[52:53]
	global_store_dwordx4 v[48:49], v[44:47], off
	s_nop 1
	s_or_b64 exec, exec, s[0:1]
	v_cvt_pk_bf16_f32 v35, v34, v35
	v_cvt_pk_bf16_f32 v34, v32, v33
	v_cvt_pk_bf16_f32 v32, v36, v37
	v_cvt_pk_bf16_f32 v33, v38, v39
	s_and_saveexec_b64 s[0:1], s[44:45]
	v_mul_u32_u24_e32 v36, s4, v158
	v_lshlrev_b32_e32 v37, v145, v192
	v_add3_u32 v212, v36, v37, v172
	v_lshl_add_u64 v[36:37], v[212:213], 1, s[52:53]
	global_store_dwordx4 v[36:37], v[32:35], off
	s_nop 1
	s_or_b64 exec, exec, s[0:1]
	s_or_b32 s4, s2, 2
	v_cvt_pk_bf16_f32 v27, v26, v27
	v_cvt_pk_bf16_f32 v26, v24, v25
	v_cvt_pk_bf16_f32 v24, v28, v29
	v_cvt_pk_bf16_f32 v25, v30, v31
	s_and_saveexec_b64 s[0:1], s[42:43]
	v_mul_u32_u24_e32 v28, s4, v159
	v_lshl_or_b32 v28, v192, v180, v28
	v_add_u32_e32 v212, v28, v181
	v_lshl_add_u64 v[28:29], v[212:213], 1, s[52:53]
	global_store_dwordx4 v[28:29], v[24:27], off
	s_nop 1
	s_or_b64 exec, exec, s[0:1]
	v_cvt_pk_bf16_f32 v19, v18, v19
	v_cvt_pk_bf16_f32 v18, v16, v17
	v_cvt_pk_bf16_f32 v16, v20, v21
	v_cvt_pk_bf16_f32 v17, v22, v23
	s_and_saveexec_b64 s[0:1], s[44:45]
	v_mul_u32_u24_e32 v20, s4, v158
	v_lshl_or_b32 v20, v192, v145, v20
	v_add_u32_e32 v212, v20, v172
	v_lshl_add_u64 v[20:21], v[212:213], 1, s[52:53]
	global_store_dwordx4 v[20:21], v[16:19], off
	s_nop 1
	s_or_b64 exec, exec, s[0:1]
	s_or_b32 s2, s2, 3
	v_cvt_pk_bf16_f32 v11, v10, v11
	v_cvt_pk_bf16_f32 v10, v8, v9
	v_cvt_pk_bf16_f32 v8, v12, v13
	v_cvt_pk_bf16_f32 v9, v14, v15
	s_and_saveexec_b64 s[0:1], s[42:43]
	v_mul_u32_u24_e32 v12, s2, v159
	v_lshlrev_b32_e32 v13, v180, v192
	v_add3_u32 v212, v12, v13, v181
	v_lshl_add_u64 v[12:13], v[212:213], 1, s[52:53]
	global_store_dwordx4 v[12:13], v[8:11], off
	s_nop 1
	s_or_b64 exec, exec, s[0:1]
	s_and_b64 vcc, exec, s[38:39]
	v_cvt_pk_bf16_f32 v3, v2, v3
	v_cvt_pk_bf16_f32 v2, v0, v1
	v_cvt_pk_bf16_f32 v0, v4, v5
	v_cvt_pk_bf16_f32 v1, v6, v7
	s_and_saveexec_b64 s[0:1], s[44:45]
	v_mul_u32_u24_e32 v4, s2, v158
	v_lshlrev_b32_e32 v5, v145, v192
	v_add3_u32 v212, v4, v5, v172
	v_lshl_add_u64 v[4:5], v[212:213], 1, s[52:53]
	global_store_dwordx4 v[4:5], v[0:3], off
	s_nop 1
	s_branch .LBB0_464
.Lepiz_m1:
	s_and_b64 vcc, exec, s[80:81]
	v_or_b32_e32 v62, s8, v192
	v_lshlrev_b32_e32 v40, 2, v40
	v_add_lshl_u32 v212, v40, s54, 2
	v_lshlrev_b32_e32 v42, 8, v62
	v_lshl_add_u64 v[40:41], s[50:51], 0, v[212:213]
	v_and_b32_e32 v212, 0xfcf00, v42
	v_lshl_add_u64 v[42:43], v[40:41], 0, v[212:213]
	v_add_co_u32_e32 v60, vcc, 0x1000, v42
	s_movk_i32 s0, 0x2000
	s_nop 0
	v_addc_co_u32_e32 v61, vcc, 0, v43, vcc
	global_load_dwordx4 v[156:159], v[42:43], off
	global_load_dwordx4 v[152:155], v[60:61], off
	v_add_co_u32_e32 v60, vcc, s0, v42
	s_nop 1
	v_addc_co_u32_e32 v61, vcc, 0, v43, vcc
	v_add_co_u32_e32 v42, vcc, 0x3000, v42
	s_nop 1
	v_addc_co_u32_e32 v43, vcc, 0, v43, vcc
	global_load_dwordx4 v[140:143], v[60:61], off
	global_load_dwordx4 v[120:123], v[42:43], off
	v_mov_b32_e32 v42, 0x2000
	v_lshl_add_u32 v42, v62, 6, v42
	v_and_b32_e32 v42, 0x3f3c0, v42
	v_lshlrev_b32_e32 v212, 2, v42
	v_lshl_add_u64 v[40:41], v[40:41], 0, v[212:213]
	v_add_co_u32_e32 v42, vcc, s0, v40
	s_movk_i32 s0, 0x3000
	s_nop 0
	v_addc_co_u32_e32 v43, vcc, 0, v41, vcc
	global_load_dwordx4 v[80:83], v[42:43], off offset:-4096
	global_load_dwordx4 v[60:63], v[42:43], off
	v_add_co_u32_e32 v42, vcc, s0, v40
	s_mov_b64 s[0:1], 0
	s_nop 0
	v_addc_co_u32_e32 v43, vcc, 0, v41, vcc
	global_load_dwordx4 v[100:103], v[40:41], off
	s_nop 0
	global_load_dwordx4 v[40:43], v[42:43], off
	v_cndmask_b32_e64 v172, 0, 1, s[80:81]
	v_cmp_ne_u32_e64 s[40:41], 1, v172
	s_waitcnt vmcnt(0)
	v_cvt_f32_f16_e32 v174, v156
	v_cvt_f32_f16_e32 v175, v157
	v_cvt_f32_f16_e32 v172, v158
	v_cvt_f32_f16_e32 v173, v159
	v_cvt_f32_f16_sdwa v176, v156 dst_sel:DWORD dst_unused:UNUSED_PAD src0_sel:WORD_1
	v_cvt_f32_f16_sdwa v177, v157 dst_sel:DWORD dst_unused:UNUSED_PAD src0_sel:WORD_1
	v_cvt_f32_f16_sdwa v158, v158 dst_sel:DWORD dst_unused:UNUSED_PAD src0_sel:WORD_1
	v_cvt_f32_f16_sdwa v157, v159 dst_sel:DWORD dst_unused:UNUSED_PAD src0_sel:WORD_1
	v_pk_mul_f32 v[206:207], v[148:149], v[176:177] op_sel:[1,0] op_sel_hi:[0,0]
	v_mov_b32_e32 v180, v175
	v_mov_b32_e32 v181, v177
	v_mul_f32_e32 v156, v151, v177
	v_pk_fma_f32 v[178:179], v[148:149], v[174:175], v[206:207] op_sel_hi:[1,0,1]
	v_pk_fma_f32 v[180:181], v[150:151], v[180:181], v[156:157] op_sel_hi:[1,1,0] neg_lo:[0,0,1] neg_hi:[0,0,1]
	v_mov_b32_e32 v182, v177
	v_mov_b32_e32 v183, v175
	v_mul_f32_e32 v156, v151, v175
	v_pk_fma_f32 v[182:183], v[150:151], v[182:183], v[156:157] op_sel_hi:[1,1,0]
	v_mov_b32_e32 v156, v173
	v_mul_f32_e32 v178, v147, v157
	v_pk_mul_f32 v[208:209], v[148:149], v[174:175]
	v_pk_mul_f32 v[210:211], v[144:145], v[158:159] op_sel:[1,0] op_sel_hi:[0,0]
	v_pk_mul_f32 v[224:225], v[144:145], v[172:173]
	v_pk_fma_f32 v[186:187], v[146:147], v[156:157], v[178:179] op_sel_hi:[1,1,0] neg_lo:[0,0,1] neg_hi:[0,0,1]
	v_mov_b32_e32 v188, v157
	v_mov_b32_e32 v189, v173
	v_mul_f32_e32 v156, v147, v173
	v_pk_fma_f32 v[184:185], v[144:145], v[172:173], v[210:211] op_sel_hi:[1,0,1]
	v_pk_fma_f32 v[188:189], v[146:147], v[188:189], v[156:157] op_sel_hi:[1,1,0]
	v_sub_f32_e32 v156, v208, v206
	v_sub_f32_e32 v178, v224, v210
	s_mov_b64 s[4:5], 0
	v_cndmask_b32_e64 v159, 0, 1, s[0:1]
	v_cmp_ne_u32_e64 s[38:39], 1, v159
	s_lshr_b32 s0, s8, 4
	s_and_b32 s4, s0, 0xfc
	s_ashr_i32 s0, s2, 31
	s_lshr_b32 s0, s0, 28
	s_add_i32 s0, s2, s0
	s_ashr_i32 s13, s0, 4
	v_add_u32_e32 v144, v204, v201
	s_movk_i32 s0, 0x300
	v_mul_lo_u32 v144, v144, s0
	v_sub_u32_e32 v144, v193, v144
	v_cndmask_b32_e64 v146, v203, v144, s[42:43]
	v_lshrrev_b32_e32 v144, 7, v146
	v_mad_u64_u32 v[144:145], s[0:1], v202, s13, v[144:145]
	v_lshlrev_b32_e32 v145, 4, v146
	v_lshl_add_u32 v144, v144, 19, v200
	v_and_b32_e32 v145, 0x600, v145
	v_and_b32_e32 v146, 31, v146
	v_or3_b32 v146, v144, v145, v146
	v_add_u32_e32 v144, 0xfffff200, v193
	v_mul_hi_i32 v145, v144, s6
	v_lshrrev_b32_e32 v147, 31, v145
	v_ashrrev_i32_e32 v145, 6, v145
	v_add_u32_e32 v145, v145, v147
	v_mul_i32_i24_e32 v147, 0x180, v145
	v_sub_u32_e32 v144, v144, v147
	v_mul_i32_i24_e32 v147, 0x2aab, v144
	v_mov_b32_e32 v148, 4
	v_ashrrev_i16_sdwa v148, v148, v147 dst_sel:DWORD dst_unused:UNUSED_PAD src0_sel:DWORD src1_sel:WORD_1
	v_lshrrev_b32_e32 v147, 31, v147
	v_add_u16_e32 v147, v148, v147
	v_mul_lo_u16_e32 v148, 0x60, v147
	v_sub_u16_e32 v144, v144, v148
	s_lshl_b32 s5, s13, 2
	v_bfe_i32 v148, v144, 0, 16
	v_mul_i32_i24_e32 v144, 0x600000, v145
	v_and_or_b32 v144, v148, 31, v144
	v_add_u32_e32 v145, s5, v147
	s_mov_b32 s0, 0x60000
	v_lshlrev_b32_e32 v147, 4, v148
	v_mad_u64_u32 v[144:145], s[0:1], v145, s0, v[144:145]
	v_and_b32_e32 v147, 0xfffffe00, v147
	s_mov_b32 s0, 0x3800000
	v_add3_u32 v147, v144, v147, s0
	v_add_u32_e32 v144, 0xffffef00, v193
	v_mul_hi_i32 v145, v144, s6
	v_lshrrev_b32_e32 v148, 31, v145
	v_ashrrev_i32_e32 v145, 7, v145
	v_add_u32_e32 v145, v145, v148
	v_mul_i32_i24_e32 v148, 0x300, v145
	v_sub_u32_e32 v144, v144, v148
	v_mul_i32_i24_e32 v148, 0x2aab, v144
	v_mov_b32_e32 v149, 5
	v_ashrrev_i16_sdwa v149, v149, v148 dst_sel:DWORD dst_unused:UNUSED_PAD src0_sel:DWORD src1_sel:WORD_1
	v_lshrrev_b32_e32 v148, 31, v148
	v_add_u16_e32 v148, v149, v148
	v_mul_lo_u16_e32 v149, 0xc0, v148
	v_sub_u16_e32 v144, v144, v149
	s_mov_b32 s0, 0xc00000
	v_bfe_i32 v149, v144, 0, 16
	v_mul_lo_u32 v144, v145, s0
	v_and_or_b32 v144, v149, 31, v144
	v_add_u32_e32 v145, s5, v148
	s_mov_b32 s0, 0xc0000
	v_lshlrev_b32_e32 v148, 4, v149
	v_mad_u64_u32 v[144:145], s[0:1], v145, s0, v[144:145]
	v_and_b32_e32 v148, 0xfffffe00, v148
	s_mov_b32 s0, 0x4400000
	v_add3_u32 v144, v144, v148, s0
	s_movk_i32 s0, 0xe00
	s_lshl_b32 s2, s13, 16
	v_cmp_gt_i32_e32 vcc, s0, v193
	s_movk_i32 s0, 0x1710
	s_add_i32 s2, s2, 0x5bfe900
	v_cmp_gt_u32_e64 s[42:43], s0, v193
	s_movk_i32 s0, 0x1700
	v_add_u32_e32 v145, s2, v193
	v_cndmask_b32_e64 v149, 0, v237, s[42:43]
	v_cmp_gt_i32_e64 s[46:47], s0, v193
	s_movk_i32 s0, 0x1100
	v_cndmask_b32_e32 v148, v236, v218, vcc
	v_cndmask_b32_e64 v149, v149, v239, s[46:47]
	v_cmp_gt_i32_e64 s[42:43], s0, v193
	v_cndmask_b32_e64 v144, v145, v144, s[46:47]
	s_nop 0
	v_cndmask_b32_e64 v159, v149, v148, s[42:43]
	v_cndmask_b32_e64 v144, v144, v147, s[42:43]
	v_cndmask_b32_e32 v181, v144, v146, vcc
	v_cvt_pk_bf16_f32 v144, v156, v179
	v_cvt_pk_bf16_f32 v145, v180, v182
	v_cmp_ne_u32_e64 s[42:43], 0, v159
	v_cndmask_b32_e64 v180, 4, 5, s[46:47]
	v_cvt_pk_bf16_f32 v146, v178, v185
	v_cvt_pk_bf16_f32 v147, v186, v188
	s_and_saveexec_b64 s[0:1], s[42:43]
	v_mul_u32_u24_e32 v148, s4, v159
	v_lshl_or_b32 v148, v192, v180, v148
	v_add_u32_e32 v212, v148, v181
	v_lshl_add_u64 v[148:149], v[212:213], 1, s[52:53]
	global_store_dwordx4 v[148:149], v[144:147], off
	s_nop 1
	s_or_b64 exec, exec, s[0:1]
	s_mov_b64 s[0:1], -1
	v_pk_mul_f32 v[182:183], v[136:137], v[176:177] op_sel:[1,0] op_sel_hi:[0,0]
	v_pk_fma_f32 v[144:145], v[136:137], v[174:175], v[182:183] op_sel_hi:[1,0,1]
	v_mov_b32_e32 v176, v175
	v_mul_f32_e32 v144, v139, v177
	v_pk_mul_f32 v[184:185], v[136:137], v[174:175]
	v_pk_fma_f32 v[146:147], v[138:139], v[176:177], v[144:145] op_sel_hi:[1,1,0] neg_lo:[0,0,1] neg_hi:[0,0,1]
	v_mov_b32_e32 v174, v177
	v_mul_f32_e32 v144, v139, v175
	v_pk_fma_f32 v[148:149], v[138:139], v[174:175], v[144:145] op_sel_hi:[1,1,0]
	v_pk_mul_f32 v[174:175], v[132:133], v[158:159] op_sel:[1,0] op_sel_hi:[0,0]
	v_mov_b32_e32 v156, v173
	v_mul_f32_e32 v144, v135, v157
	v_pk_mul_f32 v[176:177], v[132:133], v[172:173]
	v_pk_fma_f32 v[150:151], v[132:133], v[172:173], v[174:175] op_sel_hi:[1,0,1]
	v_pk_fma_f32 v[178:179], v[134:135], v[156:157], v[144:145] op_sel_hi:[1,1,0] neg_lo:[0,0,1] neg_hi:[0,0,1]
	v_mov_b32_e32 v172, v157
	v_mul_f32_e32 v144, v135, v173
	v_pk_fma_f32 v[156:157], v[134:135], v[172:173], v[144:145] op_sel_hi:[1,1,0]
	v_sub_f32_e32 v144, v184, v182
	v_sub_f32_e32 v147, v176, v174
	v_add_u32_e32 v132, v198, v197
	s_movk_i32 s0, 0x300
	v_mul_lo_u32 v132, v132, s0
	v_sub_u32_e32 v132, v194, v132
	v_cndmask_b32_e64 v134, v199, v132, s[44:45]
	v_lshrrev_b32_e32 v132, 7, v134
	v_mad_u64_u32 v[132:133], s[0:1], v195, s13, v[132:133]
	v_lshlrev_b32_e32 v133, 4, v134
	v_lshl_add_u32 v132, v132, 19, v196
	v_and_b32_e32 v133, 0x600, v133
	v_and_b32_e32 v134, 31, v134
	v_or3_b32 v134, v132, v133, v134
	v_add_u32_e32 v132, 0xfffff280, v193
	v_mul_hi_i32 v133, v132, s6
	v_lshrrev_b32_e32 v135, 31, v133
	v_ashrrev_i32_e32 v133, 6, v133
	v_add_u32_e32 v133, v133, v135
	v_mul_i32_i24_e32 v135, 0x180, v133
	v_sub_u32_e32 v132, v132, v135
	v_mul_i32_i24_e32 v135, 0x2aab, v132
	v_lshrrev_b32_e32 v136, 31, v135
	v_ashrrev_i32_e32 v135, 20, v135
	v_add_u16_e32 v135, v135, v136
	v_mul_lo_u16_e32 v136, 0x60, v135
	v_sub_u16_e32 v132, v132, v136
	v_bfe_i32 v136, v132, 0, 16
	v_mul_i32_i24_e32 v132, 0x600000, v133
	v_and_or_b32 v132, v136, 31, v132
	v_add_u32_e32 v133, s5, v135
	s_mov_b32 s0, 0x60000
	v_lshlrev_b32_e32 v135, 4, v136
	v_mad_u64_u32 v[132:133], s[0:1], v133, s0, v[132:133]
	v_and_b32_e32 v135, 0xfffffe00, v135
	s_mov_b32 s0, 0x3800000
	v_add3_u32 v135, v132, v135, s0
	v_add_u32_e32 v132, 0xffffef80, v193
	v_mul_hi_i32 v133, v132, s6
	v_lshrrev_b32_e32 v136, 31, v133
	v_ashrrev_i32_e32 v133, 7, v133
	v_add_u32_e32 v133, v133, v136
	v_mul_i32_i24_e32 v136, 0x300, v133
	v_sub_u32_e32 v132, v132, v136
	v_mul_i32_i24_e32 v136, 0x2aab, v132
	v_lshrrev_b32_e32 v137, 31, v136
	v_ashrrev_i32_e32 v136, 21, v136
	v_add_u16_e32 v136, v136, v137
	v_mul_lo_u16_e32 v137, 0xc0, v136
	v_sub_u16_e32 v132, v132, v137
	s_mov_b32 s0, 0xc00000
	v_bfe_i32 v137, v132, 0, 16
	v_mul_lo_u32 v132, v133, s0
	v_and_or_b32 v132, v137, 31, v132
	v_add_u32_e32 v133, s5, v136
	s_mov_b32 s0, 0xc0000
	v_lshlrev_b32_e32 v136, 4, v137
	v_mad_u64_u32 v[132:133], s[0:1], v133, s0, v[132:133]
	v_and_b32_e32 v136, 0xfffffe00, v136
	s_mov_b32 s0, 0x4400000
	v_add3_u32 v132, v132, v136, s0
	s_movk_i32 s0, 0xd80
	v_cmp_gt_i32_e32 vcc, s0, v193
	s_movk_i32 s0, 0x1710
	v_cmp_gt_u32_e64 s[44:45], s0, v194
	s_movk_i32 s0, 0x1680
	v_add_u32_e32 v133, s2, v194
	v_cndmask_b32_e64 v137, 0, v237, s[44:45]
	v_cmp_gt_i32_e64 s[46:47], s0, v193
	s_movk_i32 s0, 0x1080
	v_cndmask_b32_e32 v136, v236, v218, vcc
	v_cndmask_b32_e64 v137, v137, v239, s[46:47]
	v_cmp_gt_i32_e64 s[44:45], s0, v193
	v_cndmask_b32_e64 v132, v133, v132, s[46:47]
	s_nop 0
	v_cndmask_b32_e64 v158, v137, v136, s[44:45]
	v_cndmask_b32_e64 v132, v132, v135, s[44:45]
	v_cndmask_b32_e32 v172, v132, v134, vcc
	v_cvt_pk_bf16_f32 v132, v144, v145
	v_cmp_ne_u32_e64 s[44:45], 0, v158
	v_cndmask_b32_e64 v145, 4, 5, s[46:47]
	v_cvt_pk_bf16_f32 v133, v146, v148
	v_cvt_pk_bf16_f32 v134, v147, v151
	v_cvt_pk_bf16_f32 v135, v178, v156
	s_and_saveexec_b64 s[0:1], s[44:45]
	v_mul_u32_u24_e32 v136, s4, v158
	v_lshl_or_b32 v136, v192, v145, v136
	v_add_u32_e32 v212, v136, v172
	v_lshl_add_u64 v[136:137], v[212:213], 1, s[52:53]
	global_store_dwordx4 v[136:137], v[132:135], off
	s_nop 1
	s_or_b64 exec, exec, s[0:1]
	v_cvt_f32_f16_e32 v136, v152
	v_cvt_f32_f16_e32 v137, v153
	v_cvt_f32_f16_e32 v132, v154
	v_cvt_f32_f16_e32 v133, v155
	v_cvt_f32_f16_sdwa v138, v152 dst_sel:DWORD dst_unused:UNUSED_PAD src0_sel:WORD_1
	v_cvt_f32_f16_sdwa v139, v153 dst_sel:DWORD dst_unused:UNUSED_PAD src0_sel:WORD_1
	v_cvt_f32_f16_sdwa v144, v154 dst_sel:DWORD dst_unused:UNUSED_PAD src0_sel:WORD_1
	v_cvt_f32_f16_sdwa v135, v155 dst_sel:DWORD dst_unused:UNUSED_PAD src0_sel:WORD_1
	v_pk_mul_f32 v[174:175], v[128:129], v[138:139] op_sel:[1,0] op_sel_hi:[0,0]
	v_mov_b32_e32 v148, v137
	v_mov_b32_e32 v149, v139
	v_mul_f32_e32 v134, v131, v139
	v_pk_fma_f32 v[146:147], v[128:129], v[136:137], v[174:175] op_sel_hi:[1,0,1]
	v_pk_fma_f32 v[148:149], v[130:131], v[148:149], v[134:135] op_sel_hi:[1,1,0] neg_lo:[0,0,1] neg_hi:[0,0,1]
	v_mov_b32_e32 v150, v139
	v_mov_b32_e32 v151, v137
	v_mul_f32_e32 v134, v131, v137
	v_pk_fma_f32 v[150:151], v[130:131], v[150:151], v[134:135] op_sel_hi:[1,1,0]
	v_mov_b32_e32 v134, v133
	v_mul_f32_e32 v146, v127, v135
	v_pk_mul_f32 v[176:177], v[128:129], v[136:137]
	v_pk_mul_f32 v[178:179], v[124:125], v[144:145] op_sel:[1,0] op_sel_hi:[0,0]
	v_pk_mul_f32 v[182:183], v[124:125], v[132:133]
	v_pk_fma_f32 v[154:155], v[126:127], v[134:135], v[146:147] op_sel_hi:[1,1,0] neg_lo:[0,0,1] neg_hi:[0,0,1]
	v_mov_b32_e32 v156, v135
	v_mov_b32_e32 v157, v133
	v_mul_f32_e32 v134, v127, v133
	v_pk_fma_f32 v[152:153], v[124:125], v[132:133], v[178:179] op_sel_hi:[1,0,1]
	v_pk_fma_f32 v[156:157], v[126:127], v[156:157], v[134:135] op_sel_hi:[1,1,0]
	v_sub_f32_e32 v134, v176, v174
	v_sub_f32_e32 v146, v182, v178
	s_or_b32 s2, s4, 1
	v_cvt_pk_bf16_f32 v124, v134, v147
	v_cvt_pk_bf16_f32 v125, v148, v150
	v_cvt_pk_bf16_f32 v126, v146, v153
	v_cvt_pk_bf16_f32 v127, v154, v156
	s_and_saveexec_b64 s[0:1], s[42:43]
	v_mul_u32_u24_e32 v128, s2, v159
	v_lshlrev_b32_e32 v129, v180, v192
	v_add3_u32 v212, v128, v129, v181
	v_lshl_add_u64 v[128:129], v[212:213], 1, s[52:53]
	global_store_dwordx4 v[128:129], v[124:127], off
	s_nop 1
	s_or_b64 exec, exec, s[0:1]
	v_pk_mul_f32 v[148:149], v[116:117], v[138:139] op_sel:[1,0] op_sel_hi:[0,0]
	v_pk_fma_f32 v[124:125], v[116:117], v[136:137], v[148:149] op_sel_hi:[1,0,1]
	v_mov_b32_e32 v138, v137
	v_mul_f32_e32 v124, v119, v139
	v_pk_mul_f32 v[150:151], v[116:117], v[136:137]
	v_pk_fma_f32 v[126:127], v[118:119], v[138:139], v[124:125] op_sel_hi:[1,1,0] neg_lo:[0,0,1] neg_hi:[0,0,1]
	v_mov_b32_e32 v136, v139
	v_mul_f32_e32 v124, v119, v137
	v_pk_fma_f32 v[128:129], v[118:119], v[136:137], v[124:125] op_sel_hi:[1,1,0]
	v_pk_mul_f32 v[136:137], v[112:113], v[144:145] op_sel:[1,0] op_sel_hi:[0,0]
	v_mov_b32_e32 v134, v133
	v_mul_f32_e32 v124, v115, v135
	v_pk_mul_f32 v[138:139], v[112:113], v[132:133]
	v_pk_fma_f32 v[130:131], v[112:113], v[132:133], v[136:137] op_sel_hi:[1,0,1]
	v_pk_fma_f32 v[146:147], v[114:115], v[134:135], v[124:125] op_sel_hi:[1,1,0] neg_lo:[0,0,1] neg_hi:[0,0,1]
	v_mov_b32_e32 v132, v135
	v_mul_f32_e32 v124, v115, v133
	v_pk_fma_f32 v[134:135], v[114:115], v[132:133], v[124:125] op_sel_hi:[1,1,0]
	v_sub_f32_e32 v124, v150, v148
	v_sub_f32_e32 v127, v138, v136
	v_cvt_pk_bf16_f32 v112, v124, v125
	v_cvt_pk_bf16_f32 v113, v126, v128
	v_cvt_pk_bf16_f32 v114, v127, v131
	v_cvt_pk_bf16_f32 v115, v146, v134
	s_and_saveexec_b64 s[0:1], s[44:45]
	v_mul_u32_u24_e32 v116, s2, v158
	v_lshlrev_b32_e32 v117, v145, v192
	v_add3_u32 v212, v116, v117, v172
	v_lshl_add_u64 v[116:117], v[212:213], 1, s[52:53]
	global_store_dwordx4 v[116:117], v[112:115], off
	s_nop 1
	s_or_b64 exec, exec, s[0:1]
	v_cvt_f32_f16_e32 v116, v140
	v_cvt_f32_f16_e32 v117, v141
	v_cvt_f32_f16_e32 v112, v142
	v_cvt_f32_f16_e32 v113, v143
	v_cvt_f32_f16_sdwa v118, v140 dst_sel:DWORD dst_unused:UNUSED_PAD src0_sel:WORD_1
	v_cvt_f32_f16_sdwa v119, v141 dst_sel:DWORD dst_unused:UNUSED_PAD src0_sel:WORD_1
	v_cvt_f32_f16_sdwa v124, v142 dst_sel:DWORD dst_unused:UNUSED_PAD src0_sel:WORD_1
	v_cvt_f32_f16_sdwa v115, v143 dst_sel:DWORD dst_unused:UNUSED_PAD src0_sel:WORD_1
	v_pk_mul_f32 v[138:139], v[108:109], v[118:119] op_sel:[1,0] op_sel_hi:[0,0]
	v_mov_b32_e32 v128, v117
	v_mov_b32_e32 v129, v119
	v_mul_f32_e32 v114, v111, v119
	v_pk_fma_f32 v[126:127], v[108:109], v[116:117], v[138:139] op_sel_hi:[1,0,1]
	v_pk_fma_f32 v[128:129], v[110:111], v[128:129], v[114:115] op_sel_hi:[1,1,0] neg_lo:[0,0,1] neg_hi:[0,0,1]
	v_mov_b32_e32 v130, v119
	v_mov_b32_e32 v131, v117
	v_mul_f32_e32 v114, v111, v117
	v_pk_fma_f32 v[130:131], v[110:111], v[130:131], v[114:115] op_sel_hi:[1,1,0]
	v_mov_b32_e32 v114, v113
	v_mul_f32_e32 v126, v107, v115
	v_pk_mul_f32 v[140:141], v[108:109], v[116:117]
	v_pk_mul_f32 v[142:143], v[104:105], v[124:125] op_sel:[1,0] op_sel_hi:[0,0]
	v_pk_mul_f32 v[146:147], v[104:105], v[112:113]
	v_pk_fma_f32 v[134:135], v[106:107], v[114:115], v[126:127] op_sel_hi:[1,1,0] neg_lo:[0,0,1] neg_hi:[0,0,1]
	v_mov_b32_e32 v136, v115
	v_mov_b32_e32 v137, v113
	v_mul_f32_e32 v114, v107, v113
	v_pk_fma_f32 v[132:133], v[104:105], v[112:113], v[142:143] op_sel_hi:[1,0,1]
	v_pk_fma_f32 v[136:137], v[106:107], v[136:137], v[114:115] op_sel_hi:[1,1,0]
	v_sub_f32_e32 v114, v140, v138
	v_sub_f32_e32 v125, v146, v142
	s_or_b32 s2, s4, 2
	v_cvt_pk_bf16_f32 v104, v114, v127
	v_cvt_pk_bf16_f32 v105, v128, v130
	v_cvt_pk_bf16_f32 v106, v125, v133
	v_cvt_pk_bf16_f32 v107, v134, v136
	s_and_saveexec_b64 s[0:1], s[42:43]
	v_mul_u32_u24_e32 v108, s2, v159
	v_lshl_or_b32 v108, v192, v180, v108
	v_add_u32_e32 v212, v108, v181
	v_lshl_add_u64 v[108:109], v[212:213], 1, s[52:53]
	global_store_dwordx4 v[108:109], v[104:107], off
	s_nop 1
	s_or_b64 exec, exec, s[0:1]
	v_pk_mul_f32 v[128:129], v[96:97], v[118:119] op_sel:[1,0] op_sel_hi:[0,0]
	v_pk_fma_f32 v[104:105], v[96:97], v[116:117], v[128:129] op_sel_hi:[1,0,1]
	v_mov_b32_e32 v118, v117
	v_mul_f32_e32 v104, v99, v119
	v_pk_mul_f32 v[130:131], v[96:97], v[116:117]
	v_pk_fma_f32 v[106:107], v[98:99], v[118:119], v[104:105] op_sel_hi:[1,1,0] neg_lo:[0,0,1] neg_hi:[0,0,1]
	v_mov_b32_e32 v116, v119
	v_mul_f32_e32 v104, v99, v117
	v_pk_fma_f32 v[108:109], v[98:99], v[116:117], v[104:105] op_sel_hi:[1,1,0]
	v_pk_mul_f32 v[116:117], v[92:93], v[124:125] op_sel:[1,0] op_sel_hi:[0,0]
	v_mov_b32_e32 v114, v113
	v_mul_f32_e32 v104, v95, v115
	v_pk_mul_f32 v[118:119], v[92:93], v[112:113]
	v_pk_fma_f32 v[110:111], v[92:93], v[112:113], v[116:117] op_sel_hi:[1,0,1]
	v_pk_fma_f32 v[126:127], v[94:95], v[114:115], v[104:105] op_sel_hi:[1,1,0] neg_lo:[0,0,1] neg_hi:[0,0,1]
	v_mov_b32_e32 v112, v115
	v_mul_f32_e32 v104, v95, v113
	v_pk_fma_f32 v[114:115], v[94:95], v[112:113], v[104:105] op_sel_hi:[1,1,0]
	v_sub_f32_e32 v104, v130, v128
	v_sub_f32_e32 v107, v118, v116
	v_cvt_pk_bf16_f32 v92, v104, v105
	v_cvt_pk_bf16_f32 v93, v106, v108
	v_cvt_pk_bf16_f32 v94, v107, v111
	v_cvt_pk_bf16_f32 v95, v126, v114
	s_and_saveexec_b64 s[0:1], s[44:45]
	v_mul_u32_u24_e32 v96, s2, v158
	v_lshl_or_b32 v96, v192, v145, v96
	v_add_u32_e32 v212, v96, v172
	v_lshl_add_u64 v[96:97], v[212:213], 1, s[52:53]
	global_store_dwordx4 v[96:97], v[92:95], off
	s_nop 1
	s_or_b64 exec, exec, s[0:1]
	v_cvt_f32_f16_e32 v96, v120
	v_cvt_f32_f16_e32 v97, v121
	v_cvt_f32_f16_e32 v92, v122
	v_cvt_f32_f16_e32 v93, v123
	v_cvt_f32_f16_sdwa v98, v120 dst_sel:DWORD dst_unused:UNUSED_PAD src0_sel:WORD_1
	v_cvt_f32_f16_sdwa v99, v121 dst_sel:DWORD dst_unused:UNUSED_PAD src0_sel:WORD_1
	v_cvt_f32_f16_sdwa v104, v122 dst_sel:DWORD dst_unused:UNUSED_PAD src0_sel:WORD_1
	v_cvt_f32_f16_sdwa v95, v123 dst_sel:DWORD dst_unused:UNUSED_PAD src0_sel:WORD_1
	v_pk_mul_f32 v[118:119], v[88:89], v[98:99] op_sel:[1,0] op_sel_hi:[0,0]
	v_mov_b32_e32 v108, v97
	v_mov_b32_e32 v109, v99
	v_mul_f32_e32 v94, v91, v99
	v_pk_fma_f32 v[106:107], v[88:89], v[96:97], v[118:119] op_sel_hi:[1,0,1]
	v_pk_fma_f32 v[108:109], v[90:91], v[108:109], v[94:95] op_sel_hi:[1,1,0] neg_lo:[0,0,1] neg_hi:[0,0,1]
	v_mov_b32_e32 v110, v99
	v_mov_b32_e32 v111, v97
	v_mul_f32_e32 v94, v91, v97
	v_pk_fma_f32 v[110:111], v[90:91], v[110:111], v[94:95] op_sel_hi:[1,1,0]
	v_mov_b32_e32 v94, v93
	v_mul_f32_e32 v106, v87, v95
	v_pk_mul_f32 v[120:121], v[88:89], v[96:97]
	v_pk_mul_f32 v[122:123], v[84:85], v[104:105] op_sel:[1,0] op_sel_hi:[0,0]
	v_pk_mul_f32 v[124:125], v[84:85], v[92:93]
	v_pk_fma_f32 v[114:115], v[86:87], v[94:95], v[106:107] op_sel_hi:[1,1,0] neg_lo:[0,0,1] neg_hi:[0,0,1]
	v_mov_b32_e32 v116, v95
	v_mov_b32_e32 v117, v93
	v_mul_f32_e32 v94, v87, v93
	v_pk_fma_f32 v[112:113], v[84:85], v[92:93], v[122:123] op_sel_hi:[1,0,1]
	v_pk_fma_f32 v[116:117], v[86:87], v[116:117], v[94:95] op_sel_hi:[1,1,0]
	v_sub_f32_e32 v94, v120, v118
	v_sub_f32_e32 v105, v124, v122
	s_or_b32 s2, s4, 3
	v_cvt_pk_bf16_f32 v84, v94, v107
	v_cvt_pk_bf16_f32 v85, v108, v110
	v_cvt_pk_bf16_f32 v86, v105, v113
	v_cvt_pk_bf16_f32 v87, v114, v116
	s_and_saveexec_b64 s[0:1], s[42:43]
	v_mul_u32_u24_e32 v88, s2, v159
	v_lshlrev_b32_e32 v89, v180, v192
	v_add3_u32 v212, v88, v89, v181
	v_lshl_add_u64 v[88:89], v[212:213], 1, s[52:53]
	global_store_dwordx4 v[88:89], v[84:87], off
	s_nop 1
	s_or_b64 exec, exec, s[0:1]
	v_pk_mul_f32 v[108:109], v[76:77], v[98:99] op_sel:[1,0] op_sel_hi:[0,0]
	v_pk_fma_f32 v[84:85], v[76:77], v[96:97], v[108:109] op_sel_hi:[1,0,1]
	v_mov_b32_e32 v98, v97
	v_mul_f32_e32 v84, v79, v99
	v_pk_mul_f32 v[110:111], v[76:77], v[96:97]
	v_pk_fma_f32 v[86:87], v[78:79], v[98:99], v[84:85] op_sel_hi:[1,1,0] neg_lo:[0,0,1] neg_hi:[0,0,1]
	v_mov_b32_e32 v96, v99
	v_mul_f32_e32 v84, v79, v97
	v_pk_fma_f32 v[88:89], v[78:79], v[96:97], v[84:85] op_sel_hi:[1,1,0]
	v_pk_mul_f32 v[96:97], v[72:73], v[104:105] op_sel:[1,0] op_sel_hi:[0,0]
	v_mov_b32_e32 v94, v93
	v_mul_f32_e32 v84, v75, v95
	v_pk_mul_f32 v[98:99], v[72:73], v[92:93]
	v_pk_fma_f32 v[90:91], v[72:73], v[92:93], v[96:97] op_sel_hi:[1,0,1]
	v_pk_fma_f32 v[106:107], v[74:75], v[94:95], v[84:85] op_sel_hi:[1,1,0] neg_lo:[0,0,1] neg_hi:[0,0,1]
	v_mov_b32_e32 v92, v95
	v_mul_f32_e32 v84, v75, v93
	v_pk_fma_f32 v[94:95], v[74:75], v[92:93], v[84:85] op_sel_hi:[1,1,0]
	v_sub_f32_e32 v84, v110, v108
	v_sub_f32_e32 v87, v98, v96
	v_cvt_pk_bf16_f32 v72, v84, v85
	v_cvt_pk_bf16_f32 v73, v86, v88
	v_cvt_pk_bf16_f32 v74, v87, v91
	v_cvt_pk_bf16_f32 v75, v106, v94
	s_and_saveexec_b64 s[0:1], s[44:45]
	v_mul_u32_u24_e32 v76, s2, v158
	v_lshlrev_b32_e32 v77, v145, v192
	v_add3_u32 v212, v76, v77, v172
	v_lshl_add_u64 v[76:77], v[212:213], 1, s[52:53]
	global_store_dwordx4 v[76:77], v[72:75], off
	s_nop 1
	s_or_b64 exec, exec, s[0:1]
	v_cvt_f32_f16_e32 v76, v100
	v_cvt_f32_f16_e32 v77, v101
	v_cvt_f32_f16_e32 v72, v102
	v_cvt_f32_f16_e32 v73, v103
	v_cvt_f32_f16_sdwa v78, v100 dst_sel:DWORD dst_unused:UNUSED_PAD src0_sel:WORD_1
	v_cvt_f32_f16_sdwa v79, v101 dst_sel:DWORD dst_unused:UNUSED_PAD src0_sel:WORD_1
	v_cvt_f32_f16_sdwa v84, v102 dst_sel:DWORD dst_unused:UNUSED_PAD src0_sel:WORD_1
	v_cvt_f32_f16_sdwa v75, v103 dst_sel:DWORD dst_unused:UNUSED_PAD src0_sel:WORD_1
	v_pk_mul_f32 v[98:99], v[68:69], v[78:79] op_sel:[1,0] op_sel_hi:[0,0]
	v_mov_b32_e32 v88, v77
	v_mov_b32_e32 v89, v79
	v_mul_f32_e32 v74, v71, v79
	v_pk_fma_f32 v[86:87], v[68:69], v[76:77], v[98:99] op_sel_hi:[1,0,1]
	v_pk_fma_f32 v[88:89], v[70:71], v[88:89], v[74:75] op_sel_hi:[1,1,0] neg_lo:[0,0,1] neg_hi:[0,0,1]
	v_mov_b32_e32 v90, v79
	v_mov_b32_e32 v91, v77
	v_mul_f32_e32 v74, v71, v77
	v_pk_fma_f32 v[90:91], v[70:71], v[90:91], v[74:75] op_sel_hi:[1,1,0]
	v_mov_b32_e32 v74, v73
	v_mul_f32_e32 v86, v67, v75
	v_pk_mul_f32 v[100:101], v[68:69], v[76:77]
	v_pk_mul_f32 v[102:103], v[64:65], v[84:85] op_sel:[1,0] op_sel_hi:[0,0]
	v_pk_mul_f32 v[104:105], v[64:65], v[72:73]
	v_pk_fma_f32 v[94:95], v[66:67], v[74:75], v[86:87] op_sel_hi:[1,1,0] neg_lo:[0,0,1] neg_hi:[0,0,1]
	v_mov_b32_e32 v96, v75
	v_mov_b32_e32 v97, v73
	v_mul_f32_e32 v74, v67, v73
	v_pk_fma_f32 v[92:93], v[64:65], v[72:73], v[102:103] op_sel_hi:[1,0,1]
	v_pk_fma_f32 v[96:97], v[66:67], v[96:97], v[74:75] op_sel_hi:[1,1,0]
	v_sub_f32_e32 v74, v100, v98
	v_sub_f32_e32 v85, v104, v102
	s_mov_b64 s[0:1], 0
	s_addk_i32 s8, 0x80
	s_lshr_b32 s0, s8, 4
	s_and_b32 s2, s0, 0xfc
	v_cvt_pk_bf16_f32 v64, v74, v87
	v_cvt_pk_bf16_f32 v65, v88, v90
	v_cvt_pk_bf16_f32 v66, v85, v93
	v_cvt_pk_bf16_f32 v67, v94, v96
	s_and_saveexec_b64 s[0:1], s[42:43]
	v_mul_u32_u24_e32 v68, s2, v159
	v_lshl_or_b32 v68, v192, v180, v68
	v_add_u32_e32 v212, v68, v181
	v_lshl_add_u64 v[68:69], v[212:213], 1, s[52:53]
	global_store_dwordx4 v[68:69], v[64:67], off
	s_nop 1
	s_or_b64 exec, exec, s[0:1]
	v_pk_mul_f32 v[88:89], v[56:57], v[78:79] op_sel:[1,0] op_sel_hi:[0,0]
	v_pk_fma_f32 v[64:65], v[56:57], v[76:77], v[88:89] op_sel_hi:[1,0,1]
	v_mov_b32_e32 v78, v77
	v_mul_f32_e32 v64, v59, v79
	v_pk_mul_f32 v[90:91], v[56:57], v[76:77]
	v_pk_fma_f32 v[66:67], v[58:59], v[78:79], v[64:65] op_sel_hi:[1,1,0] neg_lo:[0,0,1] neg_hi:[0,0,1]
	v_mov_b32_e32 v76, v79
	v_mul_f32_e32 v64, v59, v77
	v_pk_fma_f32 v[68:69], v[58:59], v[76:77], v[64:65] op_sel_hi:[1,1,0]
	v_pk_mul_f32 v[76:77], v[52:53], v[84:85] op_sel:[1,0] op_sel_hi:[0,0]
	v_mov_b32_e32 v74, v73
	v_mul_f32_e32 v64, v55, v75
	v_pk_mul_f32 v[78:79], v[52:53], v[72:73]
	v_pk_fma_f32 v[70:71], v[52:53], v[72:73], v[76:77] op_sel_hi:[1,0,1]
	v_pk_fma_f32 v[86:87], v[54:55], v[74:75], v[64:65] op_sel_hi:[1,1,0] neg_lo:[0,0,1] neg_hi:[0,0,1]
	v_mov_b32_e32 v72, v75
	v_mul_f32_e32 v64, v55, v73
	v_pk_fma_f32 v[74:75], v[54:55], v[72:73], v[64:65] op_sel_hi:[1,1,0]
	v_sub_f32_e32 v64, v90, v88
	v_sub_f32_e32 v67, v78, v76
	v_cvt_pk_bf16_f32 v52, v64, v65
	v_cvt_pk_bf16_f32 v53, v66, v68
	v_cvt_pk_bf16_f32 v54, v67, v71
	v_cvt_pk_bf16_f32 v55, v86, v74
	s_and_saveexec_b64 s[0:1], s[44:45]
	v_mul_u32_u24_e32 v56, s2, v158
	v_lshl_or_b32 v56, v192, v145, v56
	v_add_u32_e32 v212, v56, v172
	v_lshl_add_u64 v[56:57], v[212:213], 1, s[52:53]
	global_store_dwordx4 v[56:57], v[52:55], off
	s_nop 1
	s_or_b64 exec, exec, s[0:1]
	v_cvt_f32_f16_e32 v56, v80
	v_cvt_f32_f16_e32 v57, v81
	v_cvt_f32_f16_e32 v52, v82
	v_cvt_f32_f16_e32 v53, v83
	v_cvt_f32_f16_sdwa v58, v80 dst_sel:DWORD dst_unused:UNUSED_PAD src0_sel:WORD_1
	v_cvt_f32_f16_sdwa v59, v81 dst_sel:DWORD dst_unused:UNUSED_PAD src0_sel:WORD_1
	v_cvt_f32_f16_sdwa v64, v82 dst_sel:DWORD dst_unused:UNUSED_PAD src0_sel:WORD_1
	v_cvt_f32_f16_sdwa v55, v83 dst_sel:DWORD dst_unused:UNUSED_PAD src0_sel:WORD_1
	v_pk_mul_f32 v[78:79], v[48:49], v[58:59] op_sel:[1,0] op_sel_hi:[0,0]
	v_mov_b32_e32 v68, v57
	v_mov_b32_e32 v69, v59
	v_mul_f32_e32 v54, v51, v59
	v_pk_fma_f32 v[66:67], v[48:49], v[56:57], v[78:79] op_sel_hi:[1,0,1]
	v_pk_fma_f32 v[68:69], v[50:51], v[68:69], v[54:55] op_sel_hi:[1,1,0] neg_lo:[0,0,1] neg_hi:[0,0,1]
	v_mov_b32_e32 v70, v59
	v_mov_b32_e32 v71, v57
	v_mul_f32_e32 v54, v51, v57
	v_pk_fma_f32 v[70:71], v[50:51], v[70:71], v[54:55] op_sel_hi:[1,1,0]
	v_mov_b32_e32 v54, v53
	v_mul_f32_e32 v66, v47, v55
	v_pk_mul_f32 v[80:81], v[48:49], v[56:57]
	v_pk_mul_f32 v[82:83], v[44:45], v[64:65] op_sel:[1,0] op_sel_hi:[0,0]
	v_pk_mul_f32 v[84:85], v[44:45], v[52:53]
	v_pk_fma_f32 v[74:75], v[46:47], v[54:55], v[66:67] op_sel_hi:[1,1,0] neg_lo:[0,0,1] neg_hi:[0,0,1]
	v_mov_b32_e32 v76, v55
	v_mov_b32_e32 v77, v53
	v_mul_f32_e32 v54, v47, v53
	v_pk_fma_f32 v[72:73], v[44:45], v[52:53], v[82:83] op_sel_hi:[1,0,1]
	v_pk_fma_f32 v[76:77], v[46:47], v[76:77], v[54:55] op_sel_hi:[1,1,0]
	v_sub_f32_e32 v54, v80, v78
	v_sub_f32_e32 v65, v84, v82
	s_or_b32 s4, s2, 1
	v_cvt_pk_bf16_f32 v44, v54, v67
	v_cvt_pk_bf16_f32 v45, v68, v70
	v_cvt_pk_bf16_f32 v46, v65, v73
	v_cvt_pk_bf16_f32 v47, v74, v76
	s_and_saveexec_b64 s[0:1], s[42:43]
	v_mul_u32_u24_e32 v48, s4, v159
	v_lshlrev_b32_e32 v49, v180, v192
	v_add3_u32 v212, v48, v49, v181
	v_lshl_add_u64 v[48:49], v[212:213], 1, s[52:53]
	global_store_dwordx4 v[48:49], v[44:47], off
	s_nop 1
	s_or_b64 exec, exec, s[0:1]
	v_pk_mul_f32 v[68:69], v[36:37], v[58:59] op_sel:[1,0] op_sel_hi:[0,0]
	v_pk_fma_f32 v[44:45], v[36:37], v[56:57], v[68:69] op_sel_hi:[1,0,1]
	v_mov_b32_e32 v58, v57
	v_mul_f32_e32 v44, v39, v59
	v_pk_mul_f32 v[70:71], v[36:37], v[56:57]
	v_pk_fma_f32 v[46:47], v[38:39], v[58:59], v[44:45] op_sel_hi:[1,1,0] neg_lo:[0,0,1] neg_hi:[0,0,1]
	v_mov_b32_e32 v56, v59
	v_mul_f32_e32 v44, v39, v57
	v_pk_fma_f32 v[48:49], v[38:39], v[56:57], v[44:45] op_sel_hi:[1,1,0]
	v_pk_mul_f32 v[56:57], v[32:33], v[64:65] op_sel:[1,0] op_sel_hi:[0,0]
	v_mov_b32_e32 v54, v53
	v_mul_f32_e32 v44, v35, v55
	v_pk_mul_f32 v[58:59], v[32:33], v[52:53]
	v_pk_fma_f32 v[50:51], v[32:33], v[52:53], v[56:57] op_sel_hi:[1,0,1]
	v_pk_fma_f32 v[66:67], v[34:35], v[54:55], v[44:45] op_sel_hi:[1,1,0] neg_lo:[0,0,1] neg_hi:[0,0,1]
	v_mov_b32_e32 v52, v55
	v_mul_f32_e32 v44, v35, v53
	v_pk_fma_f32 v[54:55], v[34:35], v[52:53], v[44:45] op_sel_hi:[1,1,0]
	v_sub_f32_e32 v44, v70, v68
	v_sub_f32_e32 v47, v58, v56
	v_cvt_pk_bf16_f32 v32, v44, v45
	v_cvt_pk_bf16_f32 v33, v46, v48
	v_cvt_pk_bf16_f32 v34, v47, v51
	v_cvt_pk_bf16_f32 v35, v66, v54
	s_and_saveexec_b64 s[0:1], s[44:45]
	v_mul_u32_u24_e32 v36, s4, v158
	v_lshlrev_b32_e32 v37, v145, v192
	v_add3_u32 v212, v36, v37, v172
	v_lshl_add_u64 v[36:37], v[212:213], 1, s[52:53]
	global_store_dwordx4 v[36:37], v[32:35], off
	s_nop 1
	s_or_b64 exec, exec, s[0:1]
	v_cvt_f32_f16_e32 v36, v60
	v_cvt_f32_f16_e32 v37, v61
	v_cvt_f32_f16_e32 v32, v62
	v_cvt_f32_f16_e32 v33, v63
	v_cvt_f32_f16_sdwa v38, v60 dst_sel:DWORD dst_unused:UNUSED_PAD src0_sel:WORD_1
	v_cvt_f32_f16_sdwa v39, v61 dst_sel:DWORD dst_unused:UNUSED_PAD src0_sel:WORD_1
	v_cvt_f32_f16_sdwa v44, v62 dst_sel:DWORD dst_unused:UNUSED_PAD src0_sel:WORD_1
	v_cvt_f32_f16_sdwa v35, v63 dst_sel:DWORD dst_unused:UNUSED_PAD src0_sel:WORD_1
	v_pk_mul_f32 v[58:59], v[28:29], v[38:39] op_sel:[1,0] op_sel_hi:[0,0]
	v_mov_b32_e32 v48, v37
	v_mov_b32_e32 v49, v39
	v_mul_f32_e32 v34, v31, v39
	v_pk_fma_f32 v[46:47], v[28:29], v[36:37], v[58:59] op_sel_hi:[1,0,1]
	v_pk_fma_f32 v[48:49], v[30:31], v[48:49], v[34:35] op_sel_hi:[1,1,0] neg_lo:[0,0,1] neg_hi:[0,0,1]
	v_mov_b32_e32 v50, v39
	v_mov_b32_e32 v51, v37
	v_mul_f32_e32 v34, v31, v37
	v_pk_fma_f32 v[50:51], v[30:31], v[50:51], v[34:35] op_sel_hi:[1,1,0]
	v_mov_b32_e32 v34, v33
	v_mul_f32_e32 v46, v27, v35
	v_pk_mul_f32 v[60:61], v[28:29], v[36:37]
	v_pk_mul_f32 v[62:63], v[24:25], v[44:45] op_sel:[1,0] op_sel_hi:[0,0]
	v_pk_mul_f32 v[64:65], v[24:25], v[32:33]
	v_pk_fma_f32 v[54:55], v[26:27], v[34:35], v[46:47] op_sel_hi:[1,1,0] neg_lo:[0,0,1] neg_hi:[0,0,1]
	v_mov_b32_e32 v56, v35
	v_mov_b32_e32 v57, v33
	v_mul_f32_e32 v34, v27, v33
	v_pk_fma_f32 v[52:53], v[24:25], v[32:33], v[62:63] op_sel_hi:[1,0,1]
	v_pk_fma_f32 v[56:57], v[26:27], v[56:57], v[34:35] op_sel_hi:[1,1,0]
	v_sub_f32_e32 v34, v60, v58
	v_sub_f32_e32 v45, v64, v62
	s_or_b32 s4, s2, 2
	v_cvt_pk_bf16_f32 v24, v34, v47
	v_cvt_pk_bf16_f32 v25, v48, v50
	v_cvt_pk_bf16_f32 v26, v45, v53
	v_cvt_pk_bf16_f32 v27, v54, v56
	s_and_saveexec_b64 s[0:1], s[42:43]
	v_mul_u32_u24_e32 v28, s4, v159
	v_lshl_or_b32 v28, v192, v180, v28
	v_add_u32_e32 v212, v28, v181
	v_lshl_add_u64 v[28:29], v[212:213], 1, s[52:53]
	global_store_dwordx4 v[28:29], v[24:27], off
	s_nop 1
	s_or_b64 exec, exec, s[0:1]
	v_pk_mul_f32 v[48:49], v[20:21], v[38:39] op_sel:[1,0] op_sel_hi:[0,0]
	v_pk_fma_f32 v[24:25], v[20:21], v[36:37], v[48:49] op_sel_hi:[1,0,1]
	v_mov_b32_e32 v38, v37
	v_mul_f32_e32 v24, v23, v39
	v_pk_mul_f32 v[50:51], v[20:21], v[36:37]
	v_pk_fma_f32 v[26:27], v[22:23], v[38:39], v[24:25] op_sel_hi:[1,1,0] neg_lo:[0,0,1] neg_hi:[0,0,1]
	v_mov_b32_e32 v36, v39
	v_mul_f32_e32 v24, v23, v37
	v_pk_fma_f32 v[28:29], v[22:23], v[36:37], v[24:25] op_sel_hi:[1,1,0]
	v_pk_mul_f32 v[36:37], v[16:17], v[44:45] op_sel:[1,0] op_sel_hi:[0,0]
	v_mov_b32_e32 v34, v33
	v_mul_f32_e32 v24, v19, v35
	v_pk_mul_f32 v[38:39], v[16:17], v[32:33]
	v_pk_fma_f32 v[30:31], v[16:17], v[32:33], v[36:37] op_sel_hi:[1,0,1]
	v_pk_fma_f32 v[46:47], v[18:19], v[34:35], v[24:25] op_sel_hi:[1,1,0] neg_lo:[0,0,1] neg_hi:[0,0,1]
	v_mov_b32_e32 v32, v35
	v_mul_f32_e32 v24, v19, v33
	v_pk_fma_f32 v[34:35], v[18:19], v[32:33], v[24:25] op_sel_hi:[1,1,0]
	v_sub_f32_e32 v24, v50, v48
	v_sub_f32_e32 v27, v38, v36
	v_cvt_pk_bf16_f32 v16, v24, v25
	v_cvt_pk_bf16_f32 v17, v26, v28
	v_cvt_pk_bf16_f32 v18, v27, v31
	v_cvt_pk_bf16_f32 v19, v46, v34
	s_and_saveexec_b64 s[0:1], s[44:45]
	v_mul_u32_u24_e32 v20, s4, v158
	v_lshl_or_b32 v20, v192, v145, v20
	v_add_u32_e32 v212, v20, v172
	v_lshl_add_u64 v[20:21], v[212:213], 1, s[52:53]
	global_store_dwordx4 v[20:21], v[16:19], off
	s_nop 1
	s_or_b64 exec, exec, s[0:1]
	v_cvt_f32_f16_e32 v20, v40
	v_cvt_f32_f16_e32 v21, v41
	v_cvt_f32_f16_e32 v16, v42
	v_cvt_f32_f16_e32 v17, v43
	v_cvt_f32_f16_sdwa v22, v40 dst_sel:DWORD dst_unused:UNUSED_PAD src0_sel:WORD_1
	v_cvt_f32_f16_sdwa v23, v41 dst_sel:DWORD dst_unused:UNUSED_PAD src0_sel:WORD_1
	v_cvt_f32_f16_sdwa v24, v42 dst_sel:DWORD dst_unused:UNUSED_PAD src0_sel:WORD_1
	v_cvt_f32_f16_sdwa v19, v43 dst_sel:DWORD dst_unused:UNUSED_PAD src0_sel:WORD_1
	v_pk_mul_f32 v[38:39], v[12:13], v[22:23] op_sel:[1,0] op_sel_hi:[0,0]
	v_mov_b32_e32 v28, v21
	v_mov_b32_e32 v29, v23
	v_mul_f32_e32 v18, v15, v23
	v_pk_fma_f32 v[26:27], v[12:13], v[20:21], v[38:39] op_sel_hi:[1,0,1]
	v_pk_fma_f32 v[28:29], v[14:15], v[28:29], v[18:19] op_sel_hi:[1,1,0] neg_lo:[0,0,1] neg_hi:[0,0,1]
	v_mov_b32_e32 v30, v23
	v_mov_b32_e32 v31, v21
	v_mul_f32_e32 v18, v15, v21
	v_pk_fma_f32 v[30:31], v[14:15], v[30:31], v[18:19] op_sel_hi:[1,1,0]
	v_mov_b32_e32 v18, v17
	v_mul_f32_e32 v26, v11, v19
	v_pk_mul_f32 v[40:41], v[12:13], v[20:21]
	v_pk_mul_f32 v[42:43], v[8:9], v[24:25] op_sel:[1,0] op_sel_hi:[0,0]
	v_pk_mul_f32 v[44:45], v[8:9], v[16:17]
	v_pk_fma_f32 v[34:35], v[10:11], v[18:19], v[26:27] op_sel_hi:[1,1,0] neg_lo:[0,0,1] neg_hi:[0,0,1]
	v_mov_b32_e32 v36, v19
	v_mov_b32_e32 v37, v17
	v_mul_f32_e32 v18, v11, v17
	v_pk_fma_f32 v[32:33], v[8:9], v[16:17], v[42:43] op_sel_hi:[1,0,1]
	v_pk_fma_f32 v[36:37], v[10:11], v[36:37], v[18:19] op_sel_hi:[1,1,0]
	v_sub_f32_e32 v18, v40, v38
	v_sub_f32_e32 v25, v44, v42
	s_or_b32 s2, s2, 3
	v_cvt_pk_bf16_f32 v8, v18, v27
	v_cvt_pk_bf16_f32 v9, v28, v30
	v_cvt_pk_bf16_f32 v10, v25, v33
	v_cvt_pk_bf16_f32 v11, v34, v36
	s_and_saveexec_b64 s[0:1], s[42:43]
	v_mul_u32_u24_e32 v12, s2, v159
	v_lshlrev_b32_e32 v13, v180, v192
	v_add3_u32 v212, v12, v13, v181
	v_lshl_add_u64 v[12:13], v[212:213], 1, s[52:53]
	global_store_dwordx4 v[12:13], v[8:11], off
	s_nop 1
	s_or_b64 exec, exec, s[0:1]
	s_and_b64 vcc, exec, s[80:81]
	v_pk_mul_f32 v[28:29], v[4:5], v[22:23] op_sel:[1,0] op_sel_hi:[0,0]
	v_pk_fma_f32 v[8:9], v[4:5], v[20:21], v[28:29] op_sel_hi:[1,0,1]
	v_mov_b32_e32 v22, v21
	v_mul_f32_e32 v8, v7, v23
	v_pk_mul_f32 v[30:31], v[4:5], v[20:21]
	v_pk_fma_f32 v[10:11], v[6:7], v[22:23], v[8:9] op_sel_hi:[1,1,0] neg_lo:[0,0,1] neg_hi:[0,0,1]
	v_mov_b32_e32 v20, v23
	v_mul_f32_e32 v8, v7, v21
	v_pk_fma_f32 v[12:13], v[6:7], v[20:21], v[8:9] op_sel_hi:[1,1,0]
	v_pk_mul_f32 v[20:21], v[0:1], v[24:25] op_sel:[1,0] op_sel_hi:[0,0]
	v_mov_b32_e32 v18, v17
	v_mul_f32_e32 v8, v3, v19
	v_pk_mul_f32 v[22:23], v[0:1], v[16:17]
	v_pk_fma_f32 v[14:15], v[0:1], v[16:17], v[20:21] op_sel_hi:[1,0,1]
	v_pk_fma_f32 v[26:27], v[2:3], v[18:19], v[8:9] op_sel_hi:[1,1,0] neg_lo:[0,0,1] neg_hi:[0,0,1]
	v_mov_b32_e32 v16, v19
	v_mul_f32_e32 v8, v3, v17
	v_pk_fma_f32 v[18:19], v[2:3], v[16:17], v[8:9] op_sel_hi:[1,1,0]
	v_sub_f32_e32 v8, v30, v28
	v_sub_f32_e32 v11, v22, v20
	v_cvt_pk_bf16_f32 v0, v8, v9
	v_cvt_pk_bf16_f32 v1, v10, v12
	v_cvt_pk_bf16_f32 v2, v11, v15
	v_cvt_pk_bf16_f32 v3, v26, v18
	s_and_saveexec_b64 s[0:1], s[44:45]
	v_mul_u32_u24_e32 v4, s2, v158
	v_lshlrev_b32_e32 v5, v145, v192
	v_add3_u32 v212, v4, v5, v172
	v_lshl_add_u64 v[4:5], v[212:213], 1, s[52:53]
	global_store_dwordx4 v[4:5], v[0:3], off
	s_nop 1
	s_branch .LBB0_464
.Lepiz_m2:
	v_cndmask_b32_e64 v172, 0, 1, s[80:81]
	v_cmp_ne_u32_e64 s[40:41], 1, v172
	s_mov_b64 s[4:5], -1
	v_cndmask_b32_e64 v159, 0, 1, s[0:1]
	v_cmp_ne_u32_e64 s[38:39], 1, v159
	v_mul_f32_e32 v156, 0xbfb8aa3b, v148
	v_exp_f32_e32 v156, v156
	s_nop 0
	v_add_f32_e32 v156, 1.0, v156
	v_rcp_f32_e32 v178, v156
	v_mul_f32_e32 v156, 0xbfb8aa3b, v144
	v_exp_f32_e32 v156, v156
	s_nop 0
	v_add_f32_e32 v156, 1.0, v156
	v_rcp_f32_e32 v180, v156
	v_mul_f32_e32 v156, 0xbfb8aa3b, v149
	v_exp_f32_e32 v156, v156
	s_nop 0
	v_add_f32_e32 v156, 1.0, v156
	v_rcp_f32_e32 v179, v156
	v_mul_f32_e32 v156, 0xbfb8aa3b, v145
	v_exp_f32_e32 v156, v156
	v_pk_mul_f32 v[148:149], v[148:149], v[178:179]
	v_add_f32_e32 v156, 1.0, v156
	v_rcp_f32_e32 v181, v156
	v_mul_f32_e32 v156, 0xbfb8aa3b, v150
	v_exp_f32_e32 v156, v156
	v_pk_mul_f32 v[144:145], v[144:145], v[180:181]
	v_add_f32_e32 v156, 1.0, v156
	v_rcp_f32_e32 v182, v156
	v_mul_f32_e32 v156, 0xbfb8aa3b, v146
	v_exp_f32_e32 v156, v156
	s_nop 0
	v_add_f32_e32 v156, 1.0, v156
	v_rcp_f32_e32 v184, v156
	v_mul_f32_e32 v156, 0xbfb8aa3b, v151
	v_exp_f32_e32 v156, v156
	s_nop 0
	v_add_f32_e32 v156, 1.0, v156
	v_rcp_f32_e32 v183, v156
	v_mul_f32_e32 v156, 0xbfb8aa3b, v147
	v_exp_f32_e32 v156, v156
	v_pk_mul_f32 v[150:151], v[150:151], v[182:183]
	v_add_f32_e32 v156, 1.0, v156
	v_rcp_f32_e32 v185, v156
	s_nop 0
	v_pk_mul_f32 v[146:147], v[146:147], v[184:185]
	v_mov_b32_e32 v156, v148
	v_mov_b32_e32 v179, v149
	v_mov_b32_e32 v180, v150
	v_mov_b32_e32 v182, v151
	v_mov_b32_e32 v178, v144
	v_mov_b32_e32 v185, v145
	v_mov_b32_e32 v186, v146
	v_mov_b32_e32 v188, v147
	s_lshr_b32 s0, s8, 4
	s_and_b32 s4, s0, 0xfc
	s_ashr_i32 s0, s2, 31
	s_lshr_b32 s0, s0, 28
	s_add_i32 s0, s2, s0
	s_ashr_i32 s13, s0, 4
	v_add_u32_e32 v144, v204, v201
	s_movk_i32 s0, 0x300
	v_mul_lo_u32 v144, v144, s0
	v_sub_u32_e32 v144, v193, v144
	v_cndmask_b32_e64 v146, v203, v144, s[42:43]
	v_lshrrev_b32_e32 v144, 7, v146
	v_mad_u64_u32 v[144:145], s[0:1], v202, s13, v[144:145]
	v_lshlrev_b32_e32 v145, 4, v146
	v_lshl_add_u32 v144, v144, 19, v200
	v_and_b32_e32 v145, 0x600, v145
	v_and_b32_e32 v146, 31, v146
	v_or3_b32 v146, v144, v145, v146
	v_add_u32_e32 v144, 0xfffff200, v193
	v_mul_hi_i32 v145, v144, s6
	v_lshrrev_b32_e32 v147, 31, v145
	v_ashrrev_i32_e32 v145, 6, v145
	v_add_u32_e32 v145, v145, v147
	v_mul_i32_i24_e32 v147, 0x180, v145
	v_sub_u32_e32 v144, v144, v147
	v_mul_i32_i24_e32 v147, 0x2aab, v144
	v_mov_b32_e32 v148, 4
	v_ashrrev_i16_sdwa v148, v148, v147 dst_sel:DWORD dst_unused:UNUSED_PAD src0_sel:DWORD src1_sel:WORD_1
	v_lshrrev_b32_e32 v147, 31, v147
	v_add_u16_e32 v147, v148, v147
	v_mul_lo_u16_e32 v148, 0x60, v147
	v_sub_u16_e32 v144, v144, v148
	s_lshl_b32 s5, s13, 2
	v_bfe_i32 v148, v144, 0, 16
	v_mul_i32_i24_e32 v144, 0x600000, v145
	v_and_or_b32 v144, v148, 31, v144
	v_add_u32_e32 v145, s5, v147
	s_mov_b32 s0, 0x60000
	v_lshlrev_b32_e32 v147, 4, v148
	v_mad_u64_u32 v[144:145], s[0:1], v145, s0, v[144:145]
	v_and_b32_e32 v147, 0xfffffe00, v147
	s_mov_b32 s0, 0x3800000
	v_add3_u32 v147, v144, v147, s0
	v_add_u32_e32 v144, 0xffffef00, v193
	v_mul_hi_i32 v145, v144, s6
	v_lshrrev_b32_e32 v148, 31, v145
	v_ashrrev_i32_e32 v145, 7, v145
	v_add_u32_e32 v145, v145, v148
	v_mul_i32_i24_e32 v148, 0x300, v145
	v_sub_u32_e32 v144, v144, v148
	v_mul_i32_i24_e32 v148, 0x2aab, v144
	v_mov_b32_e32 v149, 5
	v_ashrrev_i16_sdwa v149, v149, v148 dst_sel:DWORD dst_unused:UNUSED_PAD src0_sel:DWORD src1_sel:WORD_1
	v_lshrrev_b32_e32 v148, 31, v148
	v_add_u16_e32 v148, v149, v148
	v_mul_lo_u16_e32 v149, 0xc0, v148
	v_sub_u16_e32 v144, v144, v149
	s_mov_b32 s0, 0xc00000
	v_bfe_i32 v149, v144, 0, 16
	v_mul_lo_u32 v144, v145, s0
	v_and_or_b32 v144, v149, 31, v144
	v_add_u32_e32 v145, s5, v148
	s_mov_b32 s0, 0xc0000
	v_lshlrev_b32_e32 v148, 4, v149
	v_mad_u64_u32 v[144:145], s[0:1], v145, s0, v[144:145]
	v_and_b32_e32 v148, 0xfffffe00, v148
	s_mov_b32 s0, 0x4400000
	v_add3_u32 v144, v144, v148, s0
	s_movk_i32 s0, 0xe00
	s_lshl_b32 s2, s13, 16
	v_cmp_gt_i32_e32 vcc, s0, v193
	s_movk_i32 s0, 0x1710
	s_add_i32 s2, s2, 0x5bfe900
	v_cmp_gt_u32_e64 s[42:43], s0, v193
	s_movk_i32 s0, 0x1700
	v_add_u32_e32 v145, s2, v193
	v_cndmask_b32_e64 v149, 0, v237, s[42:43]
	v_cmp_gt_i32_e64 s[46:47], s0, v193
	s_movk_i32 s0, 0x1100
	v_cndmask_b32_e32 v148, v236, v218, vcc
	v_cndmask_b32_e64 v149, v149, v239, s[46:47]
	v_cmp_gt_i32_e64 s[42:43], s0, v193
	v_cndmask_b32_e64 v144, v145, v144, s[46:47]
	s_nop 0
	v_cndmask_b32_e64 v159, v149, v148, s[42:43]
	v_cndmask_b32_e64 v144, v144, v147, s[42:43]
	v_cndmask_b32_e32 v181, v144, v146, vcc
	v_cvt_pk_bf16_f32 v144, v156, v179
	v_cvt_pk_bf16_f32 v145, v180, v182
	v_cmp_ne_u32_e64 s[42:43], 0, v159
	v_cndmask_b32_e64 v180, 4, 5, s[46:47]
	v_cvt_pk_bf16_f32 v146, v178, v185
	v_cvt_pk_bf16_f32 v147, v186, v188
	s_and_saveexec_b64 s[0:1], s[42:43]
	v_mul_u32_u24_e32 v148, s4, v159
	v_lshl_or_b32 v148, v192, v180, v148
	v_add_u32_e32 v212, v148, v181
	v_lshl_add_u64 v[148:149], v[212:213], 1, s[52:53]
	global_store_dwordx4 v[148:149], v[144:147], off
	s_nop 1
	s_or_b64 exec, exec, s[0:1]
	s_mov_b64 s[0:1], -1
	v_mul_f32_e32 v145, 0xbfb8aa3b, v132
	v_exp_f32_e32 v145, v145
	v_mul_f32_e32 v144, 0xbfb8aa3b, v136
	v_exp_f32_e32 v144, v144
	v_mul_f32_e32 v149, 0xbfb8aa3b, v134
	v_add_f32_e32 v145, 1.0, v145
	v_rcp_f32_e32 v146, v145
	v_mul_f32_e32 v145, 0xbfb8aa3b, v137
	v_exp_f32_e32 v145, v145
	v_add_f32_e32 v144, 1.0, v144
	v_exp_f32_e32 v149, v149
	v_rcp_f32_e32 v144, v144
	v_add_f32_e32 v145, 1.0, v145
	v_rcp_f32_e32 v145, v145
	v_add_f32_e32 v149, 1.0, v149
	v_mul_f32_e32 v147, 0xbfb8aa3b, v133
	v_mul_f32_e32 v148, 0xbfb8aa3b, v138
	v_rcp_f32_e32 v150, v149
	v_mul_f32_e32 v149, 0xbfb8aa3b, v139
	v_pk_mul_f32 v[136:137], v[136:137], v[144:145]
	v_mul_f32_e32 v144, 0xbfb8aa3b, v135
	v_exp_f32_e32 v147, v147
	v_exp_f32_e32 v148, v148
	v_exp_f32_e32 v149, v149
	v_exp_f32_e32 v144, v144
	v_add_f32_e32 v147, 1.0, v147
	v_add_f32_e32 v148, 1.0, v148
	v_add_f32_e32 v149, 1.0, v149
	v_add_f32_e32 v144, 1.0, v144
	v_rcp_f32_e32 v147, v147
	v_rcp_f32_e32 v148, v148
	v_rcp_f32_e32 v149, v149
	v_rcp_f32_e32 v151, v144
	v_pk_mul_f32 v[132:133], v[132:133], v[146:147]
	v_pk_mul_f32 v[138:139], v[138:139], v[148:149]
	v_pk_mul_f32 v[134:135], v[134:135], v[150:151]
	v_mov_b32_e32 v144, v136
	v_mov_b32_e32 v145, v137
	v_mov_b32_e32 v146, v138
	v_mov_b32_e32 v148, v139
	v_mov_b32_e32 v147, v132
	v_mov_b32_e32 v151, v133
	v_mov_b32_e32 v178, v134
	v_mov_b32_e32 v156, v135
	v_add_u32_e32 v132, v198, v197
	s_movk_i32 s0, 0x300
	v_mul_lo_u32 v132, v132, s0
	v_sub_u32_e32 v132, v194, v132
	v_cndmask_b32_e64 v134, v199, v132, s[44:45]
	v_lshrrev_b32_e32 v132, 7, v134
	v_mad_u64_u32 v[132:133], s[0:1], v195, s13, v[132:133]
	v_lshlrev_b32_e32 v133, 4, v134
	v_lshl_add_u32 v132, v132, 19, v196
	v_and_b32_e32 v133, 0x600, v133
	v_and_b32_e32 v134, 31, v134
	v_or3_b32 v134, v132, v133, v134
	v_add_u32_e32 v132, 0xfffff280, v193
	v_mul_hi_i32 v133, v132, s6
	v_lshrrev_b32_e32 v135, 31, v133
	v_ashrrev_i32_e32 v133, 6, v133
	v_add_u32_e32 v133, v133, v135
	v_mul_i32_i24_e32 v135, 0x180, v133
	v_sub_u32_e32 v132, v132, v135
	v_mul_i32_i24_e32 v135, 0x2aab, v132
	v_lshrrev_b32_e32 v136, 31, v135
	v_ashrrev_i32_e32 v135, 20, v135
	v_add_u16_e32 v135, v135, v136
	v_mul_lo_u16_e32 v136, 0x60, v135
	v_sub_u16_e32 v132, v132, v136
	v_bfe_i32 v136, v132, 0, 16
	v_mul_i32_i24_e32 v132, 0x600000, v133
	v_and_or_b32 v132, v136, 31, v132
	v_add_u32_e32 v133, s5, v135
	s_mov_b32 s0, 0x60000
	v_lshlrev_b32_e32 v135, 4, v136
	v_mad_u64_u32 v[132:133], s[0:1], v133, s0, v[132:133]
	v_and_b32_e32 v135, 0xfffffe00, v135
	s_mov_b32 s0, 0x3800000
	v_add3_u32 v135, v132, v135, s0
	v_add_u32_e32 v132, 0xffffef80, v193
	v_mul_hi_i32 v133, v132, s6
	v_lshrrev_b32_e32 v136, 31, v133
	v_ashrrev_i32_e32 v133, 7, v133
	v_add_u32_e32 v133, v133, v136
	v_mul_i32_i24_e32 v136, 0x300, v133
	v_sub_u32_e32 v132, v132, v136
	v_mul_i32_i24_e32 v136, 0x2aab, v132
	v_lshrrev_b32_e32 v137, 31, v136
	v_ashrrev_i32_e32 v136, 21, v136
	v_add_u16_e32 v136, v136, v137
	v_mul_lo_u16_e32 v137, 0xc0, v136
	v_sub_u16_e32 v132, v132, v137
	s_mov_b32 s0, 0xc00000
	v_bfe_i32 v137, v132, 0, 16
	v_mul_lo_u32 v132, v133, s0
	v_and_or_b32 v132, v137, 31, v132
	v_add_u32_e32 v133, s5, v136
	s_mov_b32 s0, 0xc0000
	v_lshlrev_b32_e32 v136, 4, v137
	v_mad_u64_u32 v[132:133], s[0:1], v133, s0, v[132:133]
	v_and_b32_e32 v136, 0xfffffe00, v136
	s_mov_b32 s0, 0x4400000
	v_add3_u32 v132, v132, v136, s0
	s_movk_i32 s0, 0xd80
	v_cmp_gt_i32_e32 vcc, s0, v193
	s_movk_i32 s0, 0x1710
	v_cmp_gt_u32_e64 s[44:45], s0, v194
	s_movk_i32 s0, 0x1680
	v_add_u32_e32 v133, s2, v194
	v_cndmask_b32_e64 v137, 0, v237, s[44:45]
	v_cmp_gt_i32_e64 s[46:47], s0, v193
	s_movk_i32 s0, 0x1080
	v_cndmask_b32_e32 v136, v236, v218, vcc
	v_cndmask_b32_e64 v137, v137, v239, s[46:47]
	v_cmp_gt_i32_e64 s[44:45], s0, v193
	v_cndmask_b32_e64 v132, v133, v132, s[46:47]
	s_nop 0
	v_cndmask_b32_e64 v158, v137, v136, s[44:45]
	v_cndmask_b32_e64 v132, v132, v135, s[44:45]
	v_cndmask_b32_e32 v172, v132, v134, vcc
	v_cvt_pk_bf16_f32 v132, v144, v145
	v_cmp_ne_u32_e64 s[44:45], 0, v158
	v_cndmask_b32_e64 v145, 4, 5, s[46:47]
	v_cvt_pk_bf16_f32 v133, v146, v148
	v_cvt_pk_bf16_f32 v134, v147, v151
	v_cvt_pk_bf16_f32 v135, v178, v156
	s_and_saveexec_b64 s[0:1], s[44:45]
	v_mul_u32_u24_e32 v136, s4, v158
	v_lshl_or_b32 v136, v192, v145, v136
	v_add_u32_e32 v212, v136, v172
	v_lshl_add_u64 v[136:137], v[212:213], 1, s[52:53]
	global_store_dwordx4 v[136:137], v[132:135], off
	s_nop 1
	s_or_b64 exec, exec, s[0:1]
	v_mul_f32_e32 v134, 0xbfb8aa3b, v128
	v_exp_f32_e32 v134, v134
	s_nop 0
	v_add_f32_e32 v134, 1.0, v134
	v_rcp_f32_e32 v146, v134
	v_mul_f32_e32 v134, 0xbfb8aa3b, v124
	v_exp_f32_e32 v134, v134
	s_nop 0
	v_add_f32_e32 v134, 1.0, v134
	v_rcp_f32_e32 v148, v134
	v_mul_f32_e32 v134, 0xbfb8aa3b, v129
	v_exp_f32_e32 v134, v134
	s_nop 0
	v_add_f32_e32 v134, 1.0, v134
	v_rcp_f32_e32 v147, v134
	v_mul_f32_e32 v134, 0xbfb8aa3b, v125
	v_exp_f32_e32 v134, v134
	v_pk_mul_f32 v[128:129], v[128:129], v[146:147]
	v_add_f32_e32 v134, 1.0, v134
	v_rcp_f32_e32 v149, v134
	v_mul_f32_e32 v134, 0xbfb8aa3b, v130
	v_exp_f32_e32 v134, v134
	v_pk_mul_f32 v[124:125], v[124:125], v[148:149]
	v_add_f32_e32 v134, 1.0, v134
	v_rcp_f32_e32 v150, v134
	v_mul_f32_e32 v134, 0xbfb8aa3b, v126
	v_exp_f32_e32 v134, v134
	s_nop 0
	v_add_f32_e32 v134, 1.0, v134
	v_rcp_f32_e32 v152, v134
	v_mul_f32_e32 v134, 0xbfb8aa3b, v131
	v_exp_f32_e32 v134, v134
	s_nop 0
	v_add_f32_e32 v134, 1.0, v134
	v_rcp_f32_e32 v151, v134
	v_mul_f32_e32 v134, 0xbfb8aa3b, v127
	v_exp_f32_e32 v134, v134
	v_pk_mul_f32 v[130:131], v[130:131], v[150:151]
	v_add_f32_e32 v134, 1.0, v134
	v_rcp_f32_e32 v153, v134
	s_nop 0
	v_pk_mul_f32 v[126:127], v[126:127], v[152:153]
	s_or_b32 s2, s4, 1
	v_cvt_pk_bf16_f32 v127, v126, v127
	v_cvt_pk_bf16_f32 v126, v124, v125
	v_cvt_pk_bf16_f32 v124, v128, v129
	v_cvt_pk_bf16_f32 v125, v130, v131
	s_and_saveexec_b64 s[0:1], s[42:43]
	v_mul_u32_u24_e32 v128, s2, v159
	v_lshlrev_b32_e32 v129, v180, v192
	v_add3_u32 v212, v128, v129, v181
	v_lshl_add_u64 v[128:129], v[212:213], 1, s[52:53]
	global_store_dwordx4 v[128:129], v[124:127], off
	s_nop 1
	s_or_b64 exec, exec, s[0:1]
	v_mul_f32_e32 v125, 0xbfb8aa3b, v112
	v_exp_f32_e32 v125, v125
	v_mul_f32_e32 v124, 0xbfb8aa3b, v116
	v_exp_f32_e32 v124, v124
	v_mul_f32_e32 v129, 0xbfb8aa3b, v114
	v_add_f32_e32 v125, 1.0, v125
	v_rcp_f32_e32 v126, v125
	v_mul_f32_e32 v125, 0xbfb8aa3b, v117
	v_exp_f32_e32 v125, v125
	v_add_f32_e32 v124, 1.0, v124
	v_exp_f32_e32 v129, v129
	v_rcp_f32_e32 v124, v124
	v_add_f32_e32 v125, 1.0, v125
	v_rcp_f32_e32 v125, v125
	v_add_f32_e32 v129, 1.0, v129
	v_mul_f32_e32 v127, 0xbfb8aa3b, v113
	v_mul_f32_e32 v128, 0xbfb8aa3b, v118
	v_rcp_f32_e32 v130, v129
	v_mul_f32_e32 v129, 0xbfb8aa3b, v119
	v_pk_mul_f32 v[116:117], v[116:117], v[124:125]
	v_mul_f32_e32 v124, 0xbfb8aa3b, v115
	v_exp_f32_e32 v127, v127
	v_exp_f32_e32 v128, v128
	v_exp_f32_e32 v129, v129
	v_exp_f32_e32 v124, v124
	v_add_f32_e32 v127, 1.0, v127
	v_add_f32_e32 v128, 1.0, v128
	v_add_f32_e32 v129, 1.0, v129
	v_add_f32_e32 v124, 1.0, v124
	v_rcp_f32_e32 v127, v127
	v_rcp_f32_e32 v128, v128
	v_rcp_f32_e32 v129, v129
	v_rcp_f32_e32 v131, v124
	v_pk_mul_f32 v[112:113], v[112:113], v[126:127]
	v_pk_mul_f32 v[118:119], v[118:119], v[128:129]
	v_pk_mul_f32 v[114:115], v[114:115], v[130:131]
	v_cvt_pk_bf16_f32 v115, v114, v115
	v_cvt_pk_bf16_f32 v114, v112, v113
	v_cvt_pk_bf16_f32 v112, v116, v117
	v_cvt_pk_bf16_f32 v113, v118, v119
	s_and_saveexec_b64 s[0:1], s[44:45]
	v_mul_u32_u24_e32 v116, s2, v158
	v_lshlrev_b32_e32 v117, v145, v192
	v_add3_u32 v212, v116, v117, v172
	v_lshl_add_u64 v[116:117], v[212:213], 1, s[52:53]
	global_store_dwordx4 v[116:117], v[112:115], off
	s_nop 1
	s_or_b64 exec, exec, s[0:1]
	v_mul_f32_e32 v114, 0xbfb8aa3b, v108
	v_exp_f32_e32 v114, v114
	s_nop 0
	v_add_f32_e32 v114, 1.0, v114
	v_rcp_f32_e32 v126, v114
	v_mul_f32_e32 v114, 0xbfb8aa3b, v104
	v_exp_f32_e32 v114, v114
	s_nop 0
	v_add_f32_e32 v114, 1.0, v114
	v_rcp_f32_e32 v128, v114
	v_mul_f32_e32 v114, 0xbfb8aa3b, v109
	v_exp_f32_e32 v114, v114
	s_nop 0
	v_add_f32_e32 v114, 1.0, v114
	v_rcp_f32_e32 v127, v114
	v_mul_f32_e32 v114, 0xbfb8aa3b, v105
	v_exp_f32_e32 v114, v114
	v_pk_mul_f32 v[108:109], v[108:109], v[126:127]
	v_add_f32_e32 v114, 1.0, v114
	v_rcp_f32_e32 v129, v114
	v_mul_f32_e32 v114, 0xbfb8aa3b, v110
	v_exp_f32_e32 v114, v114
	v_pk_mul_f32 v[104:105], v[104:105], v[128:129]
	v_add_f32_e32 v114, 1.0, v114
	v_rcp_f32_e32 v130, v114
	v_mul_f32_e32 v114, 0xbfb8aa3b, v106
	v_exp_f32_e32 v114, v114
	s_nop 0
	v_add_f32_e32 v114, 1.0, v114
	v_rcp_f32_e32 v132, v114
	v_mul_f32_e32 v114, 0xbfb8aa3b, v111
	v_exp_f32_e32 v114, v114
	s_nop 0
	v_add_f32_e32 v114, 1.0, v114
	v_rcp_f32_e32 v131, v114
	v_mul_f32_e32 v114, 0xbfb8aa3b, v107
	v_exp_f32_e32 v114, v114
	v_pk_mul_f32 v[110:111], v[110:111], v[130:131]
	v_add_f32_e32 v114, 1.0, v114
	v_rcp_f32_e32 v133, v114
	s_nop 0
	v_pk_mul_f32 v[106:107], v[106:107], v[132:133]
	s_or_b32 s2, s4, 2
	v_cvt_pk_bf16_f32 v107, v106, v107
	v_cvt_pk_bf16_f32 v106, v104, v105
	v_cvt_pk_bf16_f32 v104, v108, v109
	v_cvt_pk_bf16_f32 v105, v110, v111
	s_and_saveexec_b64 s[0:1], s[42:43]
	v_mul_u32_u24_e32 v108, s2, v159
	v_lshl_or_b32 v108, v192, v180, v108
	v_add_u32_e32 v212, v108, v181
	v_lshl_add_u64 v[108:109], v[212:213], 1, s[52:53]
	global_store_dwordx4 v[108:109], v[104:107], off
	s_nop 1
	s_or_b64 exec, exec, s[0:1]
	v_mul_f32_e32 v105, 0xbfb8aa3b, v92
	v_exp_f32_e32 v105, v105
	v_mul_f32_e32 v104, 0xbfb8aa3b, v96
	v_exp_f32_e32 v104, v104
	v_mul_f32_e32 v109, 0xbfb8aa3b, v94
	v_add_f32_e32 v105, 1.0, v105
	v_rcp_f32_e32 v106, v105
	v_mul_f32_e32 v105, 0xbfb8aa3b, v97
	v_exp_f32_e32 v105, v105
	v_add_f32_e32 v104, 1.0, v104
	v_exp_f32_e32 v109, v109
	v_rcp_f32_e32 v104, v104
	v_add_f32_e32 v105, 1.0, v105
	v_rcp_f32_e32 v105, v105
	v_add_f32_e32 v109, 1.0, v109
	v_mul_f32_e32 v107, 0xbfb8aa3b, v93
	v_mul_f32_e32 v108, 0xbfb8aa3b, v98
	v_rcp_f32_e32 v110, v109
	v_mul_f32_e32 v109, 0xbfb8aa3b, v99
	v_pk_mul_f32 v[96:97], v[96:97], v[104:105]
	v_mul_f32_e32 v104, 0xbfb8aa3b, v95
	v_exp_f32_e32 v107, v107
	v_exp_f32_e32 v108, v108
	v_exp_f32_e32 v109, v109
	v_exp_f32_e32 v104, v104
	v_add_f32_e32 v107, 1.0, v107
	v_add_f32_e32 v108, 1.0, v108
	v_add_f32_e32 v109, 1.0, v109
	v_add_f32_e32 v104, 1.0, v104
	v_rcp_f32_e32 v107, v107
	v_rcp_f32_e32 v108, v108
	v_rcp_f32_e32 v109, v109
	v_rcp_f32_e32 v111, v104
	v_pk_mul_f32 v[92:93], v[92:93], v[106:107]
	v_pk_mul_f32 v[98:99], v[98:99], v[108:109]
	v_pk_mul_f32 v[94:95], v[94:95], v[110:111]
	v_cvt_pk_bf16_f32 v95, v94, v95
	v_cvt_pk_bf16_f32 v94, v92, v93
	v_cvt_pk_bf16_f32 v92, v96, v97
	v_cvt_pk_bf16_f32 v93, v98, v99
	s_and_saveexec_b64 s[0:1], s[44:45]
	v_mul_u32_u24_e32 v96, s2, v158
	v_lshl_or_b32 v96, v192, v145, v96
	v_add_u32_e32 v212, v96, v172
	v_lshl_add_u64 v[96:97], v[212:213], 1, s[52:53]
	global_store_dwordx4 v[96:97], v[92:95], off
	s_nop 1
	s_or_b64 exec, exec, s[0:1]
	v_mul_f32_e32 v94, 0xbfb8aa3b, v88
	v_exp_f32_e32 v94, v94
	s_nop 0
	v_add_f32_e32 v94, 1.0, v94
	v_rcp_f32_e32 v106, v94
	v_mul_f32_e32 v94, 0xbfb8aa3b, v84
	v_exp_f32_e32 v94, v94
	s_nop 0
	v_add_f32_e32 v94, 1.0, v94
	v_rcp_f32_e32 v108, v94
	v_mul_f32_e32 v94, 0xbfb8aa3b, v89
	v_exp_f32_e32 v94, v94
	s_nop 0
	v_add_f32_e32 v94, 1.0, v94
	v_rcp_f32_e32 v107, v94
	v_mul_f32_e32 v94, 0xbfb8aa3b, v85
	v_exp_f32_e32 v94, v94
	v_pk_mul_f32 v[88:89], v[88:89], v[106:107]
	v_add_f32_e32 v94, 1.0, v94
	v_rcp_f32_e32 v109, v94
	v_mul_f32_e32 v94, 0xbfb8aa3b, v90
	v_exp_f32_e32 v94, v94
	v_pk_mul_f32 v[84:85], v[84:85], v[108:109]
	v_add_f32_e32 v94, 1.0, v94
	v_rcp_f32_e32 v110, v94
	v_mul_f32_e32 v94, 0xbfb8aa3b, v86
	v_exp_f32_e32 v94, v94
	s_nop 0
	v_add_f32_e32 v94, 1.0, v94
	v_rcp_f32_e32 v112, v94
	v_mul_f32_e32 v94, 0xbfb8aa3b, v91
	v_exp_f32_e32 v94, v94
	s_nop 0
	v_add_f32_e32 v94, 1.0, v94
	v_rcp_f32_e32 v111, v94
	v_mul_f32_e32 v94, 0xbfb8aa3b, v87
	v_exp_f32_e32 v94, v94
	v_pk_mul_f32 v[90:91], v[90:91], v[110:111]
	v_add_f32_e32 v94, 1.0, v94
	v_rcp_f32_e32 v113, v94
	s_nop 0
	v_pk_mul_f32 v[86:87], v[86:87], v[112:113]
	s_or_b32 s2, s4, 3
	v_cvt_pk_bf16_f32 v87, v86, v87
	v_cvt_pk_bf16_f32 v86, v84, v85
	v_cvt_pk_bf16_f32 v84, v88, v89
	v_cvt_pk_bf16_f32 v85, v90, v91
	s_and_saveexec_b64 s[0:1], s[42:43]
	v_mul_u32_u24_e32 v88, s2, v159
	v_lshlrev_b32_e32 v89, v180, v192
	v_add3_u32 v212, v88, v89, v181
	v_lshl_add_u64 v[88:89], v[212:213], 1, s[52:53]
	global_store_dwordx4 v[88:89], v[84:87], off
	s_nop 1
	s_or_b64 exec, exec, s[0:1]
	v_mul_f32_e32 v85, 0xbfb8aa3b, v72
	v_exp_f32_e32 v85, v85
	v_mul_f32_e32 v84, 0xbfb8aa3b, v76
	v_exp_f32_e32 v84, v84
	v_mul_f32_e32 v89, 0xbfb8aa3b, v74
	v_add_f32_e32 v85, 1.0, v85
	v_rcp_f32_e32 v86, v85
	v_mul_f32_e32 v85, 0xbfb8aa3b, v77
	v_exp_f32_e32 v85, v85
	v_add_f32_e32 v84, 1.0, v84
	v_exp_f32_e32 v89, v89
	v_rcp_f32_e32 v84, v84
	v_add_f32_e32 v85, 1.0, v85
	v_rcp_f32_e32 v85, v85
	v_add_f32_e32 v89, 1.0, v89
	v_mul_f32_e32 v87, 0xbfb8aa3b, v73
	v_mul_f32_e32 v88, 0xbfb8aa3b, v78
	v_rcp_f32_e32 v90, v89
	v_mul_f32_e32 v89, 0xbfb8aa3b, v79
	v_pk_mul_f32 v[76:77], v[76:77], v[84:85]
	v_mul_f32_e32 v84, 0xbfb8aa3b, v75
	v_exp_f32_e32 v87, v87
	v_exp_f32_e32 v88, v88
	v_exp_f32_e32 v89, v89
	v_exp_f32_e32 v84, v84
	v_add_f32_e32 v87, 1.0, v87
	v_add_f32_e32 v88, 1.0, v88
	v_add_f32_e32 v89, 1.0, v89
	v_add_f32_e32 v84, 1.0, v84
	v_rcp_f32_e32 v87, v87
	v_rcp_f32_e32 v88, v88
	v_rcp_f32_e32 v89, v89
	v_rcp_f32_e32 v91, v84
	v_pk_mul_f32 v[72:73], v[72:73], v[86:87]
	v_pk_mul_f32 v[78:79], v[78:79], v[88:89]
	v_pk_mul_f32 v[74:75], v[74:75], v[90:91]
	v_cvt_pk_bf16_f32 v75, v74, v75
	v_cvt_pk_bf16_f32 v74, v72, v73
	v_cvt_pk_bf16_f32 v72, v76, v77
	v_cvt_pk_bf16_f32 v73, v78, v79
	s_and_saveexec_b64 s[0:1], s[44:45]
	v_mul_u32_u24_e32 v76, s2, v158
	v_lshlrev_b32_e32 v77, v145, v192
	v_add3_u32 v212, v76, v77, v172
	v_lshl_add_u64 v[76:77], v[212:213], 1, s[52:53]
	global_store_dwordx4 v[76:77], v[72:75], off
	s_nop 1
	s_or_b64 exec, exec, s[0:1]
	s_mov_b64 s[0:1], -1
	v_mul_f32_e32 v74, 0xbfb8aa3b, v68
	v_exp_f32_e32 v74, v74
	s_nop 0
	v_add_f32_e32 v74, 1.0, v74
	v_rcp_f32_e32 v86, v74
	v_mul_f32_e32 v74, 0xbfb8aa3b, v64
	v_exp_f32_e32 v74, v74
	s_nop 0
	v_add_f32_e32 v74, 1.0, v74
	v_rcp_f32_e32 v88, v74
	v_mul_f32_e32 v74, 0xbfb8aa3b, v69
	v_exp_f32_e32 v74, v74
	s_nop 0
	v_add_f32_e32 v74, 1.0, v74
	v_rcp_f32_e32 v87, v74
	v_mul_f32_e32 v74, 0xbfb8aa3b, v65
	v_exp_f32_e32 v74, v74
	v_pk_mul_f32 v[68:69], v[68:69], v[86:87]
	v_add_f32_e32 v74, 1.0, v74
	v_rcp_f32_e32 v89, v74
	v_mul_f32_e32 v74, 0xbfb8aa3b, v70
	v_exp_f32_e32 v74, v74
	v_pk_mul_f32 v[64:65], v[64:65], v[88:89]
	v_add_f32_e32 v74, 1.0, v74
	v_rcp_f32_e32 v90, v74
	v_mul_f32_e32 v74, 0xbfb8aa3b, v66
	v_exp_f32_e32 v74, v74
	s_nop 0
	v_add_f32_e32 v74, 1.0, v74
	v_rcp_f32_e32 v92, v74
	v_mul_f32_e32 v74, 0xbfb8aa3b, v71
	v_exp_f32_e32 v74, v74
	s_nop 0
	v_add_f32_e32 v74, 1.0, v74
	v_rcp_f32_e32 v91, v74
	v_mul_f32_e32 v74, 0xbfb8aa3b, v67
	v_exp_f32_e32 v74, v74
	v_pk_mul_f32 v[70:71], v[70:71], v[90:91]
	v_add_f32_e32 v74, 1.0, v74
	v_rcp_f32_e32 v93, v74
	s_nop 0
	v_pk_mul_f32 v[66:67], v[66:67], v[92:93]
	s_addk_i32 s8, 0x80
	s_lshr_b32 s0, s8, 4
	s_and_b32 s2, s0, 0xfc
	v_cvt_pk_bf16_f32 v67, v66, v67
	v_cvt_pk_bf16_f32 v66, v64, v65
	v_cvt_pk_bf16_f32 v64, v68, v69
	v_cvt_pk_bf16_f32 v65, v70, v71
	s_and_saveexec_b64 s[0:1], s[42:43]
	v_mul_u32_u24_e32 v68, s2, v159
	v_lshl_or_b32 v68, v192, v180, v68
	v_add_u32_e32 v212, v68, v181
	v_lshl_add_u64 v[68:69], v[212:213], 1, s[52:53]
	global_store_dwordx4 v[68:69], v[64:67], off
	s_nop 1
	s_or_b64 exec, exec, s[0:1]
	v_mul_f32_e32 v65, 0xbfb8aa3b, v52
	v_exp_f32_e32 v65, v65
	v_mul_f32_e32 v64, 0xbfb8aa3b, v56
	v_exp_f32_e32 v64, v64
	v_mul_f32_e32 v69, 0xbfb8aa3b, v54
	v_add_f32_e32 v65, 1.0, v65
	v_rcp_f32_e32 v66, v65
	v_mul_f32_e32 v65, 0xbfb8aa3b, v57
	v_exp_f32_e32 v65, v65
	v_add_f32_e32 v64, 1.0, v64
	v_exp_f32_e32 v69, v69
	v_rcp_f32_e32 v64, v64
	v_add_f32_e32 v65, 1.0, v65
	v_rcp_f32_e32 v65, v65
	v_add_f32_e32 v69, 1.0, v69
	v_mul_f32_e32 v67, 0xbfb8aa3b, v53
	v_mul_f32_e32 v68, 0xbfb8aa3b, v58
	v_rcp_f32_e32 v70, v69
	v_mul_f32_e32 v69, 0xbfb8aa3b, v59
	v_pk_mul_f32 v[56:57], v[56:57], v[64:65]
	v_mul_f32_e32 v64, 0xbfb8aa3b, v55
	v_exp_f32_e32 v67, v67
	v_exp_f32_e32 v68, v68
	v_exp_f32_e32 v69, v69
	v_exp_f32_e32 v64, v64
	v_add_f32_e32 v67, 1.0, v67
	v_add_f32_e32 v68, 1.0, v68
	v_add_f32_e32 v69, 1.0, v69
	v_add_f32_e32 v64, 1.0, v64
	v_rcp_f32_e32 v67, v67
	v_rcp_f32_e32 v68, v68
	v_rcp_f32_e32 v69, v69
	v_rcp_f32_e32 v71, v64
	v_pk_mul_f32 v[52:53], v[52:53], v[66:67]
	v_pk_mul_f32 v[58:59], v[58:59], v[68:69]
	v_pk_mul_f32 v[54:55], v[54:55], v[70:71]
	v_cvt_pk_bf16_f32 v55, v54, v55
	v_cvt_pk_bf16_f32 v54, v52, v53
	v_cvt_pk_bf16_f32 v52, v56, v57
	v_cvt_pk_bf16_f32 v53, v58, v59
	s_and_saveexec_b64 s[0:1], s[44:45]
	v_mul_u32_u24_e32 v56, s2, v158
	v_lshl_or_b32 v56, v192, v145, v56
	v_add_u32_e32 v212, v56, v172
	v_lshl_add_u64 v[56:57], v[212:213], 1, s[52:53]
	global_store_dwordx4 v[56:57], v[52:55], off
	s_nop 1
	s_or_b64 exec, exec, s[0:1]
	v_mul_f32_e32 v54, 0xbfb8aa3b, v48
	v_exp_f32_e32 v54, v54
	s_nop 0
	v_add_f32_e32 v54, 1.0, v54
	v_rcp_f32_e32 v66, v54
	v_mul_f32_e32 v54, 0xbfb8aa3b, v44
	v_exp_f32_e32 v54, v54
	s_nop 0
	v_add_f32_e32 v54, 1.0, v54
	v_rcp_f32_e32 v68, v54
	v_mul_f32_e32 v54, 0xbfb8aa3b, v49
	v_exp_f32_e32 v54, v54
	s_nop 0
	v_add_f32_e32 v54, 1.0, v54
	v_rcp_f32_e32 v67, v54
	v_mul_f32_e32 v54, 0xbfb8aa3b, v45
	v_exp_f32_e32 v54, v54
	v_pk_mul_f32 v[48:49], v[48:49], v[66:67]
	v_add_f32_e32 v54, 1.0, v54
	v_rcp_f32_e32 v69, v54
	v_mul_f32_e32 v54, 0xbfb8aa3b, v50
	v_exp_f32_e32 v54, v54
	v_pk_mul_f32 v[44:45], v[44:45], v[68:69]
	v_add_f32_e32 v54, 1.0, v54
	v_rcp_f32_e32 v70, v54
	v_mul_f32_e32 v54, 0xbfb8aa3b, v46
	v_exp_f32_e32 v54, v54
	s_nop 0
	v_add_f32_e32 v54, 1.0, v54
	v_rcp_f32_e32 v72, v54
	v_mul_f32_e32 v54, 0xbfb8aa3b, v51
	v_exp_f32_e32 v54, v54
	s_nop 0
	v_add_f32_e32 v54, 1.0, v54
	v_rcp_f32_e32 v71, v54
	v_mul_f32_e32 v54, 0xbfb8aa3b, v47
	v_exp_f32_e32 v54, v54
	v_pk_mul_f32 v[50:51], v[50:51], v[70:71]
	v_add_f32_e32 v54, 1.0, v54
	v_rcp_f32_e32 v73, v54
	s_nop 0
	v_pk_mul_f32 v[46:47], v[46:47], v[72:73]
	s_or_b32 s4, s2, 1
	v_cvt_pk_bf16_f32 v47, v46, v47
	v_cvt_pk_bf16_f32 v46, v44, v45
	v_cvt_pk_bf16_f32 v44, v48, v49
	v_cvt_pk_bf16_f32 v45, v50, v51
	s_and_saveexec_b64 s[0:1], s[42:43]
	v_mul_u32_u24_e32 v48, s4, v159
	v_lshlrev_b32_e32 v49, v180, v192
	v_add3_u32 v212, v48, v49, v181
	v_lshl_add_u64 v[48:49], v[212:213], 1, s[52:53]
	global_store_dwordx4 v[48:49], v[44:47], off
	s_nop 1
	s_or_b64 exec, exec, s[0:1]
	v_mul_f32_e32 v45, 0xbfb8aa3b, v32
	v_exp_f32_e32 v45, v45
	v_mul_f32_e32 v44, 0xbfb8aa3b, v36
	v_exp_f32_e32 v44, v44
	v_mul_f32_e32 v49, 0xbfb8aa3b, v34
	v_add_f32_e32 v45, 1.0, v45
	v_rcp_f32_e32 v46, v45
	v_mul_f32_e32 v45, 0xbfb8aa3b, v37
	v_exp_f32_e32 v45, v45
	v_add_f32_e32 v44, 1.0, v44
	v_exp_f32_e32 v49, v49
	v_rcp_f32_e32 v44, v44
	v_add_f32_e32 v45, 1.0, v45
	v_rcp_f32_e32 v45, v45
	v_add_f32_e32 v49, 1.0, v49
	v_mul_f32_e32 v47, 0xbfb8aa3b, v33
	v_mul_f32_e32 v48, 0xbfb8aa3b, v38
	v_rcp_f32_e32 v50, v49
	v_mul_f32_e32 v49, 0xbfb8aa3b, v39
	v_pk_mul_f32 v[36:37], v[36:37], v[44:45]
	v_mul_f32_e32 v44, 0xbfb8aa3b, v35
	v_exp_f32_e32 v47, v47
	v_exp_f32_e32 v48, v48
	v_exp_f32_e32 v49, v49
	v_exp_f32_e32 v44, v44
	v_add_f32_e32 v47, 1.0, v47
	v_add_f32_e32 v48, 1.0, v48
	v_add_f32_e32 v49, 1.0, v49
	v_add_f32_e32 v44, 1.0, v44
	v_rcp_f32_e32 v47, v47
	v_rcp_f32_e32 v48, v48
	v_rcp_f32_e32 v49, v49
	v_rcp_f32_e32 v51, v44
	v_pk_mul_f32 v[32:33], v[32:33], v[46:47]
	v_pk_mul_f32 v[38:39], v[38:39], v[48:49]
	v_pk_mul_f32 v[34:35], v[34:35], v[50:51]
	v_cvt_pk_bf16_f32 v35, v34, v35
	v_cvt_pk_bf16_f32 v34, v32, v33
	v_cvt_pk_bf16_f32 v32, v36, v37
	v_cvt_pk_bf16_f32 v33, v38, v39
	s_and_saveexec_b64 s[0:1], s[44:45]
	v_mul_u32_u24_e32 v36, s4, v158
	v_lshlrev_b32_e32 v37, v145, v192
	v_add3_u32 v212, v36, v37, v172
	v_lshl_add_u64 v[36:37], v[212:213], 1, s[52:53]
	global_store_dwordx4 v[36:37], v[32:35], off
	s_nop 1
	s_or_b64 exec, exec, s[0:1]
	v_mul_f32_e32 v34, 0xbfb8aa3b, v28
	v_exp_f32_e32 v34, v34
	s_nop 0
	v_add_f32_e32 v34, 1.0, v34
	v_rcp_f32_e32 v46, v34
	v_mul_f32_e32 v34, 0xbfb8aa3b, v24
	v_exp_f32_e32 v34, v34
	s_nop 0
	v_add_f32_e32 v34, 1.0, v34
	v_rcp_f32_e32 v48, v34
	v_mul_f32_e32 v34, 0xbfb8aa3b, v29
	v_exp_f32_e32 v34, v34
	s_nop 0
	v_add_f32_e32 v34, 1.0, v34
	v_rcp_f32_e32 v47, v34
	v_mul_f32_e32 v34, 0xbfb8aa3b, v25
	v_exp_f32_e32 v34, v34
	v_pk_mul_f32 v[28:29], v[28:29], v[46:47]
	v_add_f32_e32 v34, 1.0, v34
	v_rcp_f32_e32 v49, v34
	v_mul_f32_e32 v34, 0xbfb8aa3b, v30
	v_exp_f32_e32 v34, v34
	v_pk_mul_f32 v[24:25], v[24:25], v[48:49]
	v_add_f32_e32 v34, 1.0, v34
	v_rcp_f32_e32 v50, v34
	v_mul_f32_e32 v34, 0xbfb8aa3b, v26
	v_exp_f32_e32 v34, v34
	s_nop 0
	v_add_f32_e32 v34, 1.0, v34
	v_rcp_f32_e32 v52, v34
	v_mul_f32_e32 v34, 0xbfb8aa3b, v31
	v_exp_f32_e32 v34, v34
	s_nop 0
	v_add_f32_e32 v34, 1.0, v34
	v_rcp_f32_e32 v51, v34
	v_mul_f32_e32 v34, 0xbfb8aa3b, v27
	v_exp_f32_e32 v34, v34
	v_pk_mul_f32 v[30:31], v[30:31], v[50:51]
	v_add_f32_e32 v34, 1.0, v34
	v_rcp_f32_e32 v53, v34
	s_nop 0
	v_pk_mul_f32 v[26:27], v[26:27], v[52:53]
	s_or_b32 s4, s2, 2
	v_cvt_pk_bf16_f32 v27, v26, v27
	v_cvt_pk_bf16_f32 v26, v24, v25
	v_cvt_pk_bf16_f32 v24, v28, v29
	v_cvt_pk_bf16_f32 v25, v30, v31
	s_and_saveexec_b64 s[0:1], s[42:43]
	v_mul_u32_u24_e32 v28, s4, v159
	v_lshl_or_b32 v28, v192, v180, v28
	v_add_u32_e32 v212, v28, v181
	v_lshl_add_u64 v[28:29], v[212:213], 1, s[52:53]
	global_store_dwordx4 v[28:29], v[24:27], off
	s_nop 1
	s_or_b64 exec, exec, s[0:1]
	v_mul_f32_e32 v25, 0xbfb8aa3b, v16
	v_exp_f32_e32 v25, v25
	v_mul_f32_e32 v24, 0xbfb8aa3b, v20
	v_exp_f32_e32 v24, v24
	v_mul_f32_e32 v29, 0xbfb8aa3b, v18
	v_add_f32_e32 v25, 1.0, v25
	v_rcp_f32_e32 v26, v25
	v_mul_f32_e32 v25, 0xbfb8aa3b, v21
	v_exp_f32_e32 v25, v25
	v_add_f32_e32 v24, 1.0, v24
	v_exp_f32_e32 v29, v29
	v_rcp_f32_e32 v24, v24
	v_add_f32_e32 v25, 1.0, v25
	v_rcp_f32_e32 v25, v25
	v_add_f32_e32 v29, 1.0, v29
	v_mul_f32_e32 v27, 0xbfb8aa3b, v17
	v_mul_f32_e32 v28, 0xbfb8aa3b, v22
	v_rcp_f32_e32 v30, v29
	v_mul_f32_e32 v29, 0xbfb8aa3b, v23
	v_pk_mul_f32 v[20:21], v[20:21], v[24:25]
	v_mul_f32_e32 v24, 0xbfb8aa3b, v19
	v_exp_f32_e32 v27, v27
	v_exp_f32_e32 v28, v28
	v_exp_f32_e32 v29, v29
	v_exp_f32_e32 v24, v24
	v_add_f32_e32 v27, 1.0, v27
	v_add_f32_e32 v28, 1.0, v28
	v_add_f32_e32 v29, 1.0, v29
	v_add_f32_e32 v24, 1.0, v24
	v_rcp_f32_e32 v27, v27
	v_rcp_f32_e32 v28, v28
	v_rcp_f32_e32 v29, v29
	v_rcp_f32_e32 v31, v24
	v_pk_mul_f32 v[16:17], v[16:17], v[26:27]
	v_pk_mul_f32 v[22:23], v[22:23], v[28:29]
	v_pk_mul_f32 v[18:19], v[18:19], v[30:31]
	v_cvt_pk_bf16_f32 v19, v18, v19
	v_cvt_pk_bf16_f32 v18, v16, v17
	v_cvt_pk_bf16_f32 v16, v20, v21
	v_cvt_pk_bf16_f32 v17, v22, v23
	s_and_saveexec_b64 s[0:1], s[44:45]
	v_mul_u32_u24_e32 v20, s4, v158
	v_lshl_or_b32 v20, v192, v145, v20
	v_add_u32_e32 v212, v20, v172
	v_lshl_add_u64 v[20:21], v[212:213], 1, s[52:53]
	global_store_dwordx4 v[20:21], v[16:19], off
	s_nop 1
	s_or_b64 exec, exec, s[0:1]
	v_mul_f32_e32 v18, 0xbfb8aa3b, v12
	v_exp_f32_e32 v18, v18
	s_nop 0
	v_add_f32_e32 v18, 1.0, v18
	v_rcp_f32_e32 v26, v18
	v_mul_f32_e32 v18, 0xbfb8aa3b, v8
	v_exp_f32_e32 v18, v18
	s_nop 0
	v_add_f32_e32 v18, 1.0, v18
	v_rcp_f32_e32 v28, v18
	v_mul_f32_e32 v18, 0xbfb8aa3b, v13
	v_exp_f32_e32 v18, v18
	s_nop 0
	v_add_f32_e32 v18, 1.0, v18
	v_rcp_f32_e32 v27, v18
	v_mul_f32_e32 v18, 0xbfb8aa3b, v9
	v_exp_f32_e32 v18, v18
	v_pk_mul_f32 v[12:13], v[12:13], v[26:27]
	v_add_f32_e32 v18, 1.0, v18
	v_rcp_f32_e32 v29, v18
	v_mul_f32_e32 v18, 0xbfb8aa3b, v14
	v_exp_f32_e32 v18, v18
	v_pk_mul_f32 v[8:9], v[8:9], v[28:29]
	v_add_f32_e32 v18, 1.0, v18
	v_rcp_f32_e32 v30, v18
	v_mul_f32_e32 v18, 0xbfb8aa3b, v10
	v_exp_f32_e32 v18, v18
	s_nop 0
	v_add_f32_e32 v18, 1.0, v18
	v_rcp_f32_e32 v32, v18
	v_mul_f32_e32 v18, 0xbfb8aa3b, v15
	v_exp_f32_e32 v18, v18
	s_nop 0
	v_add_f32_e32 v18, 1.0, v18
	v_rcp_f32_e32 v31, v18
	v_mul_f32_e32 v18, 0xbfb8aa3b, v11
	v_exp_f32_e32 v18, v18
	v_pk_mul_f32 v[14:15], v[14:15], v[30:31]
	v_add_f32_e32 v18, 1.0, v18
	v_rcp_f32_e32 v33, v18
	s_nop 0
	v_pk_mul_f32 v[10:11], v[10:11], v[32:33]
	s_or_b32 s2, s2, 3
	v_cvt_pk_bf16_f32 v11, v10, v11
	v_cvt_pk_bf16_f32 v10, v8, v9
	v_cvt_pk_bf16_f32 v8, v12, v13
	v_cvt_pk_bf16_f32 v9, v14, v15
	s_and_saveexec_b64 s[0:1], s[42:43]
	v_mul_u32_u24_e32 v12, s2, v159
	v_lshlrev_b32_e32 v13, v180, v192
	v_add3_u32 v212, v12, v13, v181
	v_lshl_add_u64 v[12:13], v[212:213], 1, s[52:53]
	global_store_dwordx4 v[12:13], v[8:11], off
	s_nop 1
	s_or_b64 exec, exec, s[0:1]
	s_and_b64 vcc, exec, s[38:39]
	v_mul_f32_e32 v9, 0xbfb8aa3b, v0
	v_exp_f32_e32 v9, v9
	v_mul_f32_e32 v8, 0xbfb8aa3b, v4
	v_exp_f32_e32 v8, v8
	v_mul_f32_e32 v13, 0xbfb8aa3b, v2
	v_add_f32_e32 v9, 1.0, v9
	v_rcp_f32_e32 v10, v9
	v_mul_f32_e32 v9, 0xbfb8aa3b, v5
	v_exp_f32_e32 v9, v9
	v_add_f32_e32 v8, 1.0, v8
	v_exp_f32_e32 v13, v13
	v_rcp_f32_e32 v8, v8
	v_add_f32_e32 v9, 1.0, v9
	v_rcp_f32_e32 v9, v9
	v_add_f32_e32 v13, 1.0, v13
	v_mul_f32_e32 v11, 0xbfb8aa3b, v1
	v_mul_f32_e32 v12, 0xbfb8aa3b, v6
	v_rcp_f32_e32 v14, v13
	v_mul_f32_e32 v13, 0xbfb8aa3b, v7
	v_pk_mul_f32 v[4:5], v[4:5], v[8:9]
	v_mul_f32_e32 v8, 0xbfb8aa3b, v3
	v_exp_f32_e32 v11, v11
	v_exp_f32_e32 v12, v12
	v_exp_f32_e32 v13, v13
	v_exp_f32_e32 v8, v8
	v_add_f32_e32 v11, 1.0, v11
	v_add_f32_e32 v12, 1.0, v12
	v_add_f32_e32 v13, 1.0, v13
	v_add_f32_e32 v8, 1.0, v8
	v_rcp_f32_e32 v11, v11
	v_rcp_f32_e32 v12, v12
	v_rcp_f32_e32 v13, v13
	v_rcp_f32_e32 v15, v8
	v_pk_mul_f32 v[0:1], v[0:1], v[10:11]
	v_pk_mul_f32 v[6:7], v[6:7], v[12:13]
	v_pk_mul_f32 v[2:3], v[2:3], v[14:15]
	v_cvt_pk_bf16_f32 v3, v2, v3
	v_cvt_pk_bf16_f32 v2, v0, v1
	v_cvt_pk_bf16_f32 v0, v4, v5
	v_cvt_pk_bf16_f32 v1, v6, v7
	s_and_saveexec_b64 s[0:1], s[44:45]
	v_mul_u32_u24_e32 v4, s2, v158
	v_lshlrev_b32_e32 v5, v145, v192
	v_add3_u32 v212, v4, v5, v172
	v_lshl_add_u64 v[4:5], v[212:213], 1, s[52:53]
	global_store_dwordx4 v[4:5], v[0:3], off
	s_nop 1
